# P7 gather rewritten by hand: one software-pipelined row stream, LDS reads prefetched a row ahead, gelu deferred to once per 64 experts, single M0 write per row
# speedup vs baseline: 1.0195x; 1.0195x over previous
; #define LAS __attribute__((address_space(3)))
; #define P11_CX(J, ASC0, ASC1) do { const unsigned o0_ = (unsigned)__shfl_xor((int)k0, (J)), o1_ = (unsigned)__shfl_xor((int)k1, (J)); const bool lowl_ = (lane & (J)) == 0; \
;         k0 = (lowl_ == (ASC0)) ? (k0 < o0_ ? k0 : o0_) : (k0 > o0_ ? k0 : o0_); k1 = (lowl_ == (ASC1)) ? (k1 < o1_ ? k1 : o1_) : (k1 > o1_ ? k1 : o1_); } while (0)
; DI void peer_token(LAS unsigned char* ring, const bf16* x1row, float inv2, const float* nffn, const int* ex, const float* pg, const unsigned char* U6, const unsigned char* V6,
;                    const float* usc, const float* vsc, float* orow, int lane) {
;     unsigned k0 = ((unsigned)__hip_atomic_load(ex + lane, __ATOMIC_RELAXED, __HIP_MEMORY_SCOPE_AGENT) << 7) | (unsigned)lane;
;     unsigned k1 = ((unsigned)__hip_atomic_load(ex + 64 + lane, __ATOMIC_RELAXED, __HIP_MEMORY_SCOPE_AGENT) << 7) | (unsigned)(64 + lane);
;     ...
; #pragma unroll
;     for (int kk = 2; kk <= 32; kk <<= 1) { const bool asc = (lane & kk) == 0;
; #pragma unroll
;         for (int j = kk >> 1; j >= 1; j >>= 1) P11_CX(j, asc, asc); }
; #pragma unroll
;     for (int j = 32; j >= 1; j >>= 1) P11_CX(j, true, false);
;     { const unsigned lo_ = k0 < k1 ? k0 : k1, hi_ = k0 < k1 ? k1 : k0; k0 = lo_; k1 = hi_; }
; #pragma unroll
;     for (int j = 32; j >= 1; j >>= 1) P11_CX(j, true, true);
;     ...
;     const int e_lo = (int)(k0 >> 7), e_hi = (int)(k1 >> 7);
;     const float us_lo = usc[e_lo], us_hi = usc[e_hi];
;     const float gv_lo = __hip_atomic_load(pg + (k0 & 127u), __ATOMIC_RELAXED, __HIP_MEMORY_SCOPE_AGENT) * vsc[e_lo], gv_hi = __hip_atomic_load(pg + (k1 & 127u), __ATOMIC_RELAXED, __HIP_MEMORY_SCOPE_AGENT) * vsc[e_hi];
;     f32x2 h2[32], y[32];
;     asm volatile("" : "+s"(nffn));
; #pragma unroll
;     for (int i = 0; i < 16; ++i) {
;         const v2u aw = *(const v2u*)(x1row + i * 256 + lane * 4); const f32x4 g = *(const f32x4*)(nffn + i * 256 + lane * 4);
; __global__ void __launch_bounds__(NTHREADS, 2) fwd(Args args) {
;     ...
; #pragma unroll 1
;             for (int j = 0; j < 4; ++j) { const int t = tb * 32 + wave * 4 + j;
;                 peer_token(lds + wave * (4 * RSLOT), XB + (size_t)t * DM, inv2[t], norm_ffn, experts + (size_t)t * 128, pgates + (size_t)t * 128, U8, V8, usc, vsc, out + (size_t)t * DM, lane); }
.LBB0_900:
	v_and_b32_e32 v2, 64, v118
	v_add_u32_e32 v2, 64, v2
	v_xor_b32_e32 v3, 1, v118
	v_cmp_lt_i32_e32 vcc, v3, v2
	s_waitcnt vmcnt(0)
	v_readlane_b32 s44, v249, 17
	s_add_i32 s97, s97, s44
	v_cndmask_b32_e32 v3, v118, v3, vcc
	v_lshlrev_b32_e32 v106, 2, v3
	v_xor_b32_e32 v3, 2, v118
	v_cmp_lt_i32_e32 vcc, v3, v2
	s_mov_b32 s76, 0
	s_nop 0
	v_cndmask_b32_e32 v3, v118, v3, vcc
	v_lshlrev_b32_e32 v107, 2, v3
	v_xor_b32_e32 v3, 4, v118
	v_cmp_lt_i32_e32 vcc, v3, v2
	s_barrier
	s_nop 0
	v_cndmask_b32_e32 v3, v118, v3, vcc
	v_lshlrev_b32_e32 v108, 2, v3
	v_xor_b32_e32 v3, 8, v118
	v_cmp_lt_i32_e32 vcc, v3, v2
	s_nop 1
	v_cndmask_b32_e32 v3, v118, v3, vcc
	v_lshlrev_b32_e32 v109, 2, v3
	v_xor_b32_e32 v3, 16, v118
	v_cmp_lt_i32_e32 vcc, v3, v2
	s_nop 1
	v_cndmask_b32_e32 v3, v118, v3, vcc
	v_lshlrev_b32_e32 v110, 2, v3
	v_xor_b32_e32 v3, 32, v118
	v_cmp_lt_i32_e32 vcc, v3, v2
	s_nop 1
	v_cndmask_b32_e32 v2, v118, v3, vcc
	v_lshlrev_b32_e32 v111, 2, v2
	global_load_dwordx4 v[178:181], v66, s[60:61]
	global_load_dwordx4 v[182:185], v66, s[60:61] offset:1024
	global_load_dwordx4 v[186:189], v66, s[60:61] offset:2048
	global_load_dwordx4 v[190:193], v66, s[60:61] offset:3072
	s_add_u32 s46, s60, 0x1000
	s_addc_u32 s47, s61, 0
	global_load_dwordx4 v[194:197], v66, s[46:47]
	global_load_dwordx4 v[198:201], v66, s[46:47] offset:1024
	global_load_dwordx4 v[202:205], v66, s[46:47] offset:2048
	global_load_dwordx4 v[206:209], v66, s[46:47] offset:3072
	s_add_u32 s46, s60, 0x2000
	s_addc_u32 s47, s61, 0
	global_load_dwordx4 v[210:213], v66, s[46:47]
	global_load_dwordx4 v[214:217], v66, s[46:47] offset:1024
	global_load_dwordx4 v[218:221], v66, s[46:47] offset:2048
	global_load_dwordx4 v[222:225], v66, s[46:47] offset:3072
	s_add_u32 s46, s60, 0x3000
	s_addc_u32 s47, s61, 0
	global_load_dwordx4 v[226:229], v66, s[46:47]
	global_load_dwordx4 v[230:233], v66, s[46:47] offset:1024
	global_load_dwordx4 v[234:237], v66, s[46:47] offset:2048
	global_load_dwordx4 v[238:241], v66, s[46:47] offset:3072
	v_readfirstlane_b32 s98, v72
	v_readfirstlane_b32 s47, v74
	s_sub_u32 s98, s47, s98
	v_readfirstlane_b32 s99, v73
	v_readfirstlane_b32 s47, v75
	s_subb_u32 s99, s47, s99
.LBB0_901:
	s_add_i32 s46, s76, s97
	s_ashr_i32 s47, s46, 31
	s_lshl_b64 s[44:45], s[46:47], 12
	s_lshl_b64 s[74:75], s[46:47], 2
	s_add_u32 s74, s64, s74
	s_addc_u32 s75, s65, s75
	s_lshl_b64 s[78:79], s[46:47], 9
	v_lshl_add_u64 v[2:3], v[78:79], 0, s[78:79]
	global_load_dword v96, v67, s[74:75]
	global_load_dword v4, v[2:3], off sc1
	s_nop 0
	global_load_dword v2, v[2:3], off offset:256 sc1
	s_add_u32 s74, s56, s78
	s_addc_u32 s75, s57, s79
	s_lshl_b64 s[46:47], s[46:47], 13
	v_lshl_add_u64 v[8:9], v[68:69], 0, s[46:47]
	s_mov_b64 s[46:47], 0x1000
	v_lshl_add_u64 v[18:19], v[8:9], 0, s[46:47]
	global_load_dwordx2 v[146:147], v[8:9], off
	global_load_dwordx2 v[148:149], v[8:9], off offset:512
	global_load_dwordx2 v[150:151], v[8:9], off offset:1024
	global_load_dwordx2 v[152:153], v[8:9], off offset:1536
	global_load_dwordx2 v[154:155], v[8:9], off offset:2048
	global_load_dwordx2 v[156:157], v[8:9], off offset:2560
	global_load_dwordx2 v[158:159], v[8:9], off offset:3072
	global_load_dwordx2 v[160:161], v[8:9], off offset:3584
	global_load_dwordx2 v[162:163], v[18:19], off
	global_load_dwordx2 v[164:165], v[18:19], off offset:512
	global_load_dwordx2 v[166:167], v[18:19], off offset:1024
	global_load_dwordx2 v[168:169], v[18:19], off offset:1536
	global_load_dwordx2 v[170:171], v[18:19], off offset:2048
	global_load_dwordx2 v[172:173], v[18:19], off offset:2560
	global_load_dwordx2 v[174:175], v[18:19], off offset:3072
	global_load_dwordx2 v[176:177], v[18:19], off offset:3584
	s_mov_b64 s[46:47], 0x1200
	v_lshl_add_u64 v[16:17], v[8:9], 0, s[46:47]
	s_mov_b64 s[46:47], 0x1400
	s_mov_b32 m0, s33
	s_mov_b32 s77, 9
	v_mov_b32_e32 v120, 0
	s_waitcnt vmcnt(17)
	v_lshl_or_b32 v3, v4, 7, v1
	s_waitcnt vmcnt(16)
	v_lshl_or_b32 v2, v2, 7, v114
	ds_bpermute_b32 v4, v106, v3
	ds_bpermute_b32 v5, v106, v2
	s_waitcnt lgkmcnt(1)
	v_min_u32_e32 v6, v3, v4
	v_max_u32_e32 v3, v3, v4
	s_waitcnt lgkmcnt(0)
	v_min_u32_e32 v4, v2, v5
	v_max_u32_e32 v2, v2, v5
	v_cndmask_b32_e64 v3, v3, v6, s[48:49]
	v_cndmask_b32_e64 v2, v2, v4, s[48:49]
	ds_bpermute_b32 v4, v107, v3
	ds_bpermute_b32 v5, v107, v2
	s_waitcnt lgkmcnt(1)
	v_min_u32_e32 v6, v3, v4
	v_max_u32_e32 v3, v3, v4
	s_waitcnt lgkmcnt(0)
	v_min_u32_e32 v4, v2, v5
	v_max_u32_e32 v2, v2, v5
	v_cndmask_b32_e64 v3, v3, v6, s[6:7]
	v_cndmask_b32_e64 v2, v2, v4, s[6:7]
	ds_bpermute_b32 v4, v106, v3
	ds_bpermute_b32 v5, v106, v2
	s_waitcnt lgkmcnt(1)
	v_min_u32_e32 v6, v3, v4
	v_max_u32_e32 v3, v3, v4
	s_waitcnt lgkmcnt(0)
	v_min_u32_e32 v4, v2, v5
	v_max_u32_e32 v2, v2, v5
	v_cndmask_b32_e64 v3, v3, v6, s[8:9]
	v_cndmask_b32_e64 v2, v2, v4, s[8:9]
	ds_bpermute_b32 v4, v108, v3
	ds_bpermute_b32 v5, v108, v2
	s_waitcnt lgkmcnt(1)
	v_min_u32_e32 v6, v3, v4
	v_max_u32_e32 v3, v3, v4
	s_waitcnt lgkmcnt(0)
	v_min_u32_e32 v4, v2, v5
	v_max_u32_e32 v2, v2, v5
	v_cndmask_b32_e64 v3, v3, v6, s[12:13]
	v_cndmask_b32_e64 v2, v2, v4, s[12:13]
	ds_bpermute_b32 v4, v107, v3
	ds_bpermute_b32 v5, v107, v2
	s_waitcnt lgkmcnt(1)
	v_min_u32_e32 v6, v3, v4
	v_max_u32_e32 v3, v3, v4
	s_waitcnt lgkmcnt(0)
	v_min_u32_e32 v4, v2, v5
	v_max_u32_e32 v2, v2, v5
	v_cndmask_b32_e64 v3, v3, v6, s[14:15]
	v_cndmask_b32_e64 v2, v2, v4, s[14:15]
	ds_bpermute_b32 v4, v106, v3
	ds_bpermute_b32 v5, v106, v2
	s_waitcnt lgkmcnt(1)
	v_min_u32_e32 v6, v3, v4
	v_max_u32_e32 v3, v3, v4
	s_waitcnt lgkmcnt(0)
; #define P11_CX(J, ASC0, ASC1) do { const unsigned o0_ = (unsigned)__shfl_xor((int)k0, (J)), o1_ = (unsigned)__shfl_xor((int)k1, (J)); const bool lowl_ = (lane & (J)) == 0; \
;         k0 = (lowl_ == (ASC0)) ? (k0 < o0_ ? k0 : o0_) : (k0 > o0_ ? k0 : o0_); k1 = (lowl_ == (ASC1)) ? (k1 < o1_ ? k1 : o1_) : (k1 > o1_ ? k1 : o1_); } while (0)
; DI void peer_token(LAS unsigned char* ring, const bf16* x1row, float inv2, const float* nffn, const int* ex, const float* pg, const unsigned char* U6, const unsigned char* V6,
;                    const float* usc, const float* vsc, float* orow, int lane) {
;     ...
; #pragma unroll
;     for (int kk = 2; kk <= 32; kk <<= 1) { const bool asc = (lane & kk) == 0;
; #pragma unroll
;         for (int j = kk >> 1; j >= 1; j >>= 1) P11_CX(j, asc, asc); }
; #pragma unroll
;     for (int j = 32; j >= 1; j >>= 1) P11_CX(j, true, false);
;     { const unsigned lo_ = k0 < k1 ? k0 : k1, hi_ = k0 < k1 ? k1 : k0; k0 = lo_; k1 = hi_; }
; #pragma unroll
;     for (int j = 32; j >= 1; j >>= 1) P11_CX(j, true, true);
	v_min_u32_e32 v4, v2, v5
	v_max_u32_e32 v2, v2, v5
	v_cndmask_b32_e64 v3, v3, v6, s[16:17]
	v_cndmask_b32_e64 v2, v2, v4, s[16:17]
	ds_bpermute_b32 v4, v109, v3
	ds_bpermute_b32 v5, v109, v2
	s_waitcnt lgkmcnt(1)
	v_min_u32_e32 v6, v3, v4
	v_max_u32_e32 v3, v3, v4
	s_waitcnt lgkmcnt(0)
	v_min_u32_e32 v4, v2, v5
	v_max_u32_e32 v2, v2, v5
	v_cndmask_b32_e64 v3, v3, v6, s[20:21]
	v_cndmask_b32_e64 v2, v2, v4, s[20:21]
	ds_bpermute_b32 v4, v108, v3
	ds_bpermute_b32 v5, v108, v2
	s_waitcnt lgkmcnt(1)
	v_min_u32_e32 v6, v3, v4
	v_max_u32_e32 v3, v3, v4
	s_waitcnt lgkmcnt(0)
	v_min_u32_e32 v4, v2, v5
	v_max_u32_e32 v2, v2, v5
	v_cndmask_b32_e64 v3, v3, v6, s[22:23]
	v_cndmask_b32_e64 v2, v2, v4, s[22:23]
	ds_bpermute_b32 v4, v107, v3
	ds_bpermute_b32 v5, v107, v2
	s_waitcnt lgkmcnt(1)
	v_min_u32_e32 v6, v3, v4
	v_max_u32_e32 v3, v3, v4
	s_waitcnt lgkmcnt(0)
	v_min_u32_e32 v4, v2, v5
	v_max_u32_e32 v2, v2, v5
	v_cndmask_b32_e64 v3, v3, v6, s[24:25]
	v_cndmask_b32_e64 v2, v2, v4, s[24:25]
	ds_bpermute_b32 v4, v106, v3
	ds_bpermute_b32 v5, v106, v2
	s_waitcnt lgkmcnt(1)
	v_min_u32_e32 v6, v3, v4
	v_max_u32_e32 v3, v3, v4
	s_waitcnt lgkmcnt(0)
	v_min_u32_e32 v4, v2, v5
	v_max_u32_e32 v2, v2, v5
	v_cndmask_b32_e64 v3, v3, v6, s[26:27]
	v_cndmask_b32_e64 v2, v2, v4, s[26:27]
	ds_bpermute_b32 v4, v110, v3
	ds_bpermute_b32 v5, v110, v2
	s_waitcnt lgkmcnt(1)
	v_min_u32_e32 v6, v3, v4
	v_max_u32_e32 v3, v3, v4
	s_waitcnt lgkmcnt(0)
	v_min_u32_e32 v4, v2, v5
	v_max_u32_e32 v2, v2, v5
	v_cndmask_b32_e64 v3, v3, v6, s[30:31]
	v_cndmask_b32_e64 v2, v2, v4, s[30:31]
	ds_bpermute_b32 v4, v109, v3
	ds_bpermute_b32 v5, v109, v2
	s_waitcnt lgkmcnt(1)
	v_min_u32_e32 v6, v3, v4
	v_max_u32_e32 v3, v3, v4
	s_waitcnt lgkmcnt(0)
	v_min_u32_e32 v4, v2, v5
	v_max_u32_e32 v2, v2, v5
	v_cndmask_b32_e64 v3, v3, v6, s[34:35]
	v_cndmask_b32_e64 v2, v2, v4, s[34:35]
	ds_bpermute_b32 v4, v108, v3
	ds_bpermute_b32 v5, v108, v2
	s_waitcnt lgkmcnt(1)
	v_min_u32_e32 v6, v3, v4
	v_max_u32_e32 v3, v3, v4
	s_waitcnt lgkmcnt(0)
	v_min_u32_e32 v4, v2, v5
	v_max_u32_e32 v2, v2, v5
	v_cndmask_b32_e64 v3, v3, v6, s[36:37]
	v_cndmask_b32_e64 v2, v2, v4, s[36:37]
	ds_bpermute_b32 v4, v107, v3
	ds_bpermute_b32 v5, v107, v2
	s_waitcnt lgkmcnt(1)
	v_min_u32_e32 v6, v3, v4
	v_max_u32_e32 v3, v3, v4
	s_waitcnt lgkmcnt(0)
	v_min_u32_e32 v4, v2, v5
	v_max_u32_e32 v2, v2, v5
	v_cndmask_b32_e64 v3, v3, v6, s[38:39]
	v_cndmask_b32_e64 v2, v2, v4, s[38:39]
	ds_bpermute_b32 v4, v106, v3
	ds_bpermute_b32 v5, v106, v2
	s_waitcnt lgkmcnt(0)
	v_min_u32_e32 v6, v2, v5
	v_max_u32_e32 v2, v2, v5
	v_min_u32_e32 v5, v3, v4
	v_max_u32_e32 v3, v3, v4
	v_cndmask_b32_e64 v2, v2, v6, s[40:41]
	v_cndmask_b32_e64 v3, v3, v5, s[40:41]
	ds_bpermute_b32 v4, v111, v3
	ds_bpermute_b32 v5, v111, v2
	s_waitcnt lgkmcnt(1)
	v_min_u32_e32 v6, v3, v4
	v_max_u32_e32 v3, v3, v4
	s_waitcnt lgkmcnt(0)
	v_min_u32_e32 v4, v2, v5
	v_max_u32_e32 v2, v2, v5
	v_cndmask_b32_e64 v3, v3, v6, s[42:43]
	v_cndmask_b32_e64 v2, v4, v2, s[42:43]
	ds_bpermute_b32 v4, v110, v3
	ds_bpermute_b32 v5, v110, v2
	s_waitcnt lgkmcnt(1)
	v_min_u32_e32 v6, v3, v4
	v_max_u32_e32 v3, v3, v4
	s_waitcnt lgkmcnt(0)
	v_min_u32_e32 v4, v2, v5
	v_max_u32_e32 v2, v2, v5
	v_cndmask_b32_e64 v3, v3, v6, s[28:29]
	v_cndmask_b32_e64 v2, v4, v2, s[28:29]
	ds_bpermute_b32 v4, v109, v3
	ds_bpermute_b32 v5, v109, v2
	s_waitcnt lgkmcnt(1)
	v_min_u32_e32 v6, v3, v4
	v_max_u32_e32 v3, v3, v4
	s_waitcnt lgkmcnt(0)
	v_min_u32_e32 v4, v2, v5
	v_max_u32_e32 v2, v2, v5
	v_cndmask_b32_e64 v3, v3, v6, s[18:19]
	v_cndmask_b32_e64 v2, v4, v2, s[18:19]
	ds_bpermute_b32 v4, v108, v3
	ds_bpermute_b32 v5, v108, v2
	s_waitcnt lgkmcnt(1)
	v_min_u32_e32 v6, v3, v4
	v_max_u32_e32 v3, v3, v4
	s_waitcnt lgkmcnt(0)
	v_min_u32_e32 v4, v2, v5
	v_max_u32_e32 v2, v2, v5
	v_cndmask_b32_e64 v3, v3, v6, s[10:11]
	v_cndmask_b32_e64 v2, v4, v2, s[10:11]
	ds_bpermute_b32 v4, v107, v3
	ds_bpermute_b32 v5, v107, v2
	s_waitcnt lgkmcnt(1)
	v_min_u32_e32 v6, v3, v4
	v_max_u32_e32 v3, v3, v4
	s_waitcnt lgkmcnt(0)
	v_min_u32_e32 v4, v2, v5
	v_max_u32_e32 v2, v2, v5
	v_cndmask_b32_e64 v3, v3, v6, s[4:5]
	v_cndmask_b32_e64 v2, v4, v2, s[4:5]
	ds_bpermute_b32 v4, v106, v3
	ds_bpermute_b32 v5, v106, v2
	s_waitcnt lgkmcnt(1)
	v_min_u32_e32 v6, v3, v4
	v_max_u32_e32 v3, v3, v4
	s_waitcnt lgkmcnt(0)
	v_min_u32_e32 v4, v2, v5
	v_max_u32_e32 v2, v2, v5
	v_cndmask_b32_e64 v3, v3, v6, s[0:1]
	v_cndmask_b32_e64 v2, v4, v2, s[0:1]
	v_min_u32_e32 v4, v3, v2
	v_max_u32_e32 v2, v3, v2
	ds_bpermute_b32 v3, v111, v4
	ds_bpermute_b32 v5, v111, v2
	s_waitcnt lgkmcnt(1)
	v_min_u32_e32 v6, v4, v3
	v_max_u32_e32 v3, v4, v3
	s_waitcnt lgkmcnt(0)
	v_min_u32_e32 v4, v2, v5
	v_max_u32_e32 v2, v2, v5
	v_cndmask_b32_e64 v3, v3, v6, s[42:43]
	v_cndmask_b32_e64 v2, v2, v4, s[42:43]
	ds_bpermute_b32 v4, v110, v3
	ds_bpermute_b32 v5, v110, v2
	s_waitcnt lgkmcnt(1)
	v_min_u32_e32 v6, v3, v4
	v_max_u32_e32 v3, v3, v4
	s_waitcnt lgkmcnt(0)
	v_min_u32_e32 v4, v2, v5
	v_max_u32_e32 v2, v2, v5
	v_cndmask_b32_e64 v3, v3, v6, s[28:29]
	v_cndmask_b32_e64 v2, v2, v4, s[28:29]
	ds_bpermute_b32 v4, v109, v3
	ds_bpermute_b32 v5, v109, v2
	s_waitcnt lgkmcnt(1)
	v_min_u32_e32 v6, v3, v4
	v_max_u32_e32 v3, v3, v4
	s_waitcnt lgkmcnt(0)
	v_min_u32_e32 v4, v2, v5
	v_max_u32_e32 v2, v2, v5
	v_cndmask_b32_e64 v3, v3, v6, s[18:19]
	v_cndmask_b32_e64 v2, v2, v4, s[18:19]
	ds_bpermute_b32 v4, v108, v3
	ds_bpermute_b32 v5, v108, v2
	s_waitcnt lgkmcnt(1)
	v_min_u32_e32 v6, v3, v4
	v_max_u32_e32 v3, v3, v4
	s_waitcnt lgkmcnt(0)
	v_min_u32_e32 v4, v2, v5
	v_max_u32_e32 v2, v2, v5
	v_cndmask_b32_e64 v3, v3, v6, s[10:11]
	v_cndmask_b32_e64 v2, v2, v4, s[10:11]
	ds_bpermute_b32 v4, v107, v3
	ds_bpermute_b32 v5, v107, v2
	s_waitcnt lgkmcnt(1)
; #define P11_DMA(gsrc, ldst, NP) do { _Pragma("unroll") for (int _i = 0; _i < (NP); ++_i) \
;     __builtin_amdgcn_global_load_lds((const unsigned*)((gsrc) + _i * 1024), (LAS unsigned*)((ldst) + _i * 1024), 16, 0, 0); } while (0)
; #define P11_CX(J, ASC0, ASC1) do { const unsigned o0_ = (unsigned)__shfl_xor((int)k0, (J)), o1_ = (unsigned)__shfl_xor((int)k1, (J)); const bool lowl_ = (lane & (J)) == 0; \
;         k0 = (lowl_ == (ASC0)) ? (k0 < o0_ ? k0 : o0_) : (k0 > o0_ ? k0 : o0_); k1 = (lowl_ == (ASC1)) ? (k1 < o1_ ? k1 : o1_) : (k1 > o1_ ? k1 : o1_); } while (0)
; DI void peer_token(LAS unsigned char* ring, const bf16* x1row, float inv2, const float* nffn, const int* ex, const float* pg, const unsigned char* U6, const unsigned char* V6,
;                    const float* usc, const float* vsc, float* orow, int lane) {
;     ...
;     { const unsigned lo_ = k0 < k1 ? k0 : k1, hi_ = k0 < k1 ? k1 : k0; k0 = lo_; k1 = hi_; }
; #pragma unroll
;     for (int j = 32; j >= 1; j >>= 1) P11_CX(j, true, true);
;     ...
;     const int e_lo = (int)(k0 >> 7), e_hi = (int)(k1 >> 7);
;     const float us_lo = usc[e_lo], us_hi = usc[e_hi];
;     const float gv_lo = __hip_atomic_load(pg + (k0 & 127u), __ATOMIC_RELAXED, __HIP_MEMORY_SCOPE_AGENT) * vsc[e_lo], gv_hi = __hip_atomic_load(pg + (k1 & 127u), __ATOMIC_RELAXED, __HIP_MEMORY_SCOPE_AGENT) * vsc[e_hi];
;     f32x2 h2[32], y[32];
;     asm volatile("" : "+s"(nffn));
; #pragma unroll
;     for (int i = 0; i < 16; ++i) {
;         const v2u aw = *(const v2u*)(x1row + i * 256 + lane * 4); const f32x4 g = *(const f32x4*)(nffn + i * 256 + lane * 4);
;         h2[2 * i] = (f32x2){bflo(aw.x) * inv2 * g.x, bfhi(aw.x) * inv2 * g.y}; h2[2 * i + 1] = (f32x2){bflo(aw.y) * inv2 * g.z, bfhi(aw.y) * inv2 * g.w};
;     }
; #pragma unroll
;     for (int i = 0; i < 32; ++i) y[i] = (f32x2){0.f, 0.f};
;     asm volatile("s_waitcnt vmcnt(0)" ::: "memory");
;     const unsigned char* ul = U6 + lane * 16; const unsigned char* vl = V6 + lane * 16;
;     {
; #pragma unroll
;         for (int j = 0; j < 8; ++j) { const int ej = __builtin_amdgcn_readlane(e_lo, j); P11_DMA(ul + (size_t)ej * ROW4, ring + j * ROW4, 2); }
	v_min_u32_e32 v6, v3, v4
	v_max_u32_e32 v3, v3, v4
	s_waitcnt lgkmcnt(0)
	v_min_u32_e32 v4, v2, v5
	v_max_u32_e32 v2, v2, v5
	v_cndmask_b32_e64 v3, v3, v6, s[4:5]
	v_cndmask_b32_e64 v2, v2, v4, s[4:5]
	ds_bpermute_b32 v4, v106, v3
	ds_bpermute_b32 v5, v106, v2
	s_waitcnt lgkmcnt(1)
	v_min_u32_e32 v6, v3, v4
	v_max_u32_e32 v3, v3, v4
	s_waitcnt lgkmcnt(0)
	v_min_u32_e32 v4, v2, v5
	v_max_u32_e32 v2, v2, v5
	v_cndmask_b32_e64 v3, v3, v6, s[0:1]
	v_cndmask_b32_e64 v2, v2, v4, s[0:1]
	v_lshrrev_b32_e32 v112, 7, v3
	v_lshrrev_b32_e32 v113, 7, v2
	v_and_b32_e32 v3, 0x7f, v3
	v_and_b32_e32 v2, 0x7f, v2
	v_lshlrev_b32_e32 v4, 2, v112
	v_lshlrev_b32_e32 v5, 2, v113
	v_lshlrev_b32_e32 v3, 2, v3
	v_lshlrev_b32_e32 v2, 2, v2
	global_load_dword v121, v4, s[52:53]
	global_load_dword v119, v5, s[52:53]
	global_load_dword v104, v3, s[74:75] sc1
	global_load_dword v105, v4, s[54:55]
	global_load_dword v122, v2, s[74:75] sc1
	global_load_dword v123, v5, s[54:55]
	s_mov_b64 s[74:75], s[60:61]
	s_waitcnt vmcnt(2)
	v_mul_f32_e32 v124, v105, v104
	v_lshlrev_b32_e32 v10, 16, v146
	v_and_b32_e32 v11, 0xffff0000, v146
	v_lshlrev_b32_e32 v12, 16, v147
	v_and_b32_e32 v13, 0xffff0000, v147
	v_pk_mul_f32 v[10:11], v[96:97], v[10:11] op_sel_hi:[0,1]
	v_pk_mul_f32 v[12:13], v[96:97], v[12:13] op_sel_hi:[0,1]
	v_pk_mul_f32 v[20:21], v[178:179], v[10:11]
	v_pk_mul_f32 v[22:23], v[180:181], v[12:13]
	v_lshlrev_b32_e32 v14, 16, v148
	v_and_b32_e32 v15, 0xffff0000, v148
	v_lshlrev_b32_e32 v16, 16, v149
	v_and_b32_e32 v17, 0xffff0000, v149
	v_pk_mul_f32 v[14:15], v[96:97], v[14:15] op_sel_hi:[0,1]
	v_pk_mul_f32 v[16:17], v[96:97], v[16:17] op_sel_hi:[0,1]
	v_pk_mul_f32 v[24:25], v[182:183], v[14:15]
	v_pk_mul_f32 v[26:27], v[184:185], v[16:17]
	v_lshlrev_b32_e32 v10, 16, v150
	v_and_b32_e32 v11, 0xffff0000, v150
	v_lshlrev_b32_e32 v12, 16, v151
	v_and_b32_e32 v13, 0xffff0000, v151
	v_pk_mul_f32 v[10:11], v[96:97], v[10:11] op_sel_hi:[0,1]
	v_pk_mul_f32 v[12:13], v[96:97], v[12:13] op_sel_hi:[0,1]
	v_pk_mul_f32 v[28:29], v[186:187], v[10:11]
	v_pk_mul_f32 v[30:31], v[188:189], v[12:13]
	v_lshlrev_b32_e32 v14, 16, v152
	v_and_b32_e32 v15, 0xffff0000, v152
	v_lshlrev_b32_e32 v16, 16, v153
	v_and_b32_e32 v17, 0xffff0000, v153
	v_pk_mul_f32 v[14:15], v[96:97], v[14:15] op_sel_hi:[0,1]
	v_pk_mul_f32 v[16:17], v[96:97], v[16:17] op_sel_hi:[0,1]
	v_pk_mul_f32 v[32:33], v[190:191], v[14:15]
	v_pk_mul_f32 v[34:35], v[192:193], v[16:17]
	v_lshlrev_b32_e32 v10, 16, v154
	v_and_b32_e32 v11, 0xffff0000, v154
	v_lshlrev_b32_e32 v12, 16, v155
	v_and_b32_e32 v13, 0xffff0000, v155
	v_pk_mul_f32 v[10:11], v[96:97], v[10:11] op_sel_hi:[0,1]
	v_pk_mul_f32 v[12:13], v[96:97], v[12:13] op_sel_hi:[0,1]
	v_pk_mul_f32 v[36:37], v[194:195], v[10:11]
	v_pk_mul_f32 v[38:39], v[196:197], v[12:13]
	v_lshlrev_b32_e32 v14, 16, v156
	v_and_b32_e32 v15, 0xffff0000, v156
	v_lshlrev_b32_e32 v16, 16, v157
	v_and_b32_e32 v17, 0xffff0000, v157
	v_pk_mul_f32 v[14:15], v[96:97], v[14:15] op_sel_hi:[0,1]
	v_pk_mul_f32 v[16:17], v[96:97], v[16:17] op_sel_hi:[0,1]
	v_pk_mul_f32 v[40:41], v[198:199], v[14:15]
	v_pk_mul_f32 v[42:43], v[200:201], v[16:17]
	v_lshlrev_b32_e32 v10, 16, v158
	v_and_b32_e32 v11, 0xffff0000, v158
	v_lshlrev_b32_e32 v12, 16, v159
	v_and_b32_e32 v13, 0xffff0000, v159
	v_pk_mul_f32 v[10:11], v[96:97], v[10:11] op_sel_hi:[0,1]
	v_pk_mul_f32 v[12:13], v[96:97], v[12:13] op_sel_hi:[0,1]
	v_pk_mul_f32 v[44:45], v[202:203], v[10:11]
	v_pk_mul_f32 v[46:47], v[204:205], v[12:13]
	v_lshlrev_b32_e32 v14, 16, v160
	v_and_b32_e32 v15, 0xffff0000, v160
	v_lshlrev_b32_e32 v16, 16, v161
	v_and_b32_e32 v17, 0xffff0000, v161
	v_pk_mul_f32 v[14:15], v[96:97], v[14:15] op_sel_hi:[0,1]
	v_pk_mul_f32 v[16:17], v[96:97], v[16:17] op_sel_hi:[0,1]
	v_pk_mul_f32 v[48:49], v[206:207], v[14:15]
	v_pk_mul_f32 v[50:51], v[208:209], v[16:17]
	v_lshlrev_b32_e32 v10, 16, v162
	v_and_b32_e32 v11, 0xffff0000, v162
	v_lshlrev_b32_e32 v12, 16, v163
	v_and_b32_e32 v13, 0xffff0000, v163
	v_pk_mul_f32 v[10:11], v[96:97], v[10:11] op_sel_hi:[0,1]
	v_pk_mul_f32 v[12:13], v[96:97], v[12:13] op_sel_hi:[0,1]
	v_pk_mul_f32 v[52:53], v[210:211], v[10:11]
	v_pk_mul_f32 v[54:55], v[212:213], v[12:13]
	v_lshlrev_b32_e32 v14, 16, v164
	v_and_b32_e32 v15, 0xffff0000, v164
	v_lshlrev_b32_e32 v16, 16, v165
	v_and_b32_e32 v17, 0xffff0000, v165
	v_pk_mul_f32 v[14:15], v[96:97], v[14:15] op_sel_hi:[0,1]
	v_pk_mul_f32 v[16:17], v[96:97], v[16:17] op_sel_hi:[0,1]
	v_pk_mul_f32 v[56:57], v[214:215], v[14:15]
	v_pk_mul_f32 v[58:59], v[216:217], v[16:17]
	v_lshlrev_b32_e32 v10, 16, v166
	v_and_b32_e32 v11, 0xffff0000, v166
	v_lshlrev_b32_e32 v12, 16, v167
	v_and_b32_e32 v13, 0xffff0000, v167
	v_pk_mul_f32 v[10:11], v[96:97], v[10:11] op_sel_hi:[0,1]
	v_pk_mul_f32 v[12:13], v[96:97], v[12:13] op_sel_hi:[0,1]
	v_pk_mul_f32 v[60:61], v[218:219], v[10:11]
	v_pk_mul_f32 v[62:63], v[220:221], v[12:13]
	v_lshlrev_b32_e32 v14, 16, v168
	v_and_b32_e32 v15, 0xffff0000, v168
	v_lshlrev_b32_e32 v16, 16, v169
	v_and_b32_e32 v17, 0xffff0000, v169
	v_pk_mul_f32 v[14:15], v[96:97], v[14:15] op_sel_hi:[0,1]
	v_pk_mul_f32 v[16:17], v[96:97], v[16:17] op_sel_hi:[0,1]
	v_pk_mul_f32 v[64:65], v[222:223], v[14:15]
	v_pk_mul_f32 v[80:81], v[224:225], v[16:17]
	v_lshlrev_b32_e32 v10, 16, v170
	v_and_b32_e32 v11, 0xffff0000, v170
	v_lshlrev_b32_e32 v12, 16, v171
	v_and_b32_e32 v13, 0xffff0000, v171
	v_pk_mul_f32 v[10:11], v[96:97], v[10:11] op_sel_hi:[0,1]
	v_pk_mul_f32 v[12:13], v[96:97], v[12:13] op_sel_hi:[0,1]
	v_pk_mul_f32 v[82:83], v[226:227], v[10:11]
	v_pk_mul_f32 v[84:85], v[228:229], v[12:13]
	v_lshlrev_b32_e32 v14, 16, v172
	v_and_b32_e32 v15, 0xffff0000, v172
	v_lshlrev_b32_e32 v16, 16, v173
	v_and_b32_e32 v17, 0xffff0000, v173
	v_pk_mul_f32 v[14:15], v[96:97], v[14:15] op_sel_hi:[0,1]
	v_pk_mul_f32 v[16:17], v[96:97], v[16:17] op_sel_hi:[0,1]
	v_pk_mul_f32 v[86:87], v[230:231], v[14:15]
	v_pk_mul_f32 v[88:89], v[232:233], v[16:17]
	v_lshlrev_b32_e32 v10, 16, v174
	v_and_b32_e32 v11, 0xffff0000, v174
	v_lshlrev_b32_e32 v12, 16, v175
	v_and_b32_e32 v13, 0xffff0000, v175
	v_pk_mul_f32 v[10:11], v[96:97], v[10:11] op_sel_hi:[0,1]
	v_pk_mul_f32 v[12:13], v[96:97], v[12:13] op_sel_hi:[0,1]
	v_pk_mul_f32 v[90:91], v[234:235], v[10:11]
	v_pk_mul_f32 v[92:93], v[236:237], v[12:13]
	v_lshlrev_b32_e32 v14, 16, v176
	v_and_b32_e32 v15, 0xffff0000, v176
	v_lshlrev_b32_e32 v16, 16, v177
	v_and_b32_e32 v17, 0xffff0000, v177
	v_pk_mul_f32 v[14:15], v[96:97], v[14:15] op_sel_hi:[0,1]
	v_pk_mul_f32 v[16:17], v[96:97], v[16:17] op_sel_hi:[0,1]
	v_pk_mul_f32 v[94:95], v[238:239], v[14:15]
	v_pk_mul_f32 v[96:97], v[240:241], v[16:17]
	v_readlane_b32 s46, v112, 0
	s_ashr_i32 s47, s46, 31
	s_lshl_b64 s[46:47], s[46:47], 11
	v_readlane_b32 s74, v112, 2
	s_ashr_i32 s75, s74, 31
	s_lshl_b64 s[74:75], s[74:75], 11
	s_waitcnt vmcnt(0)
; #define P11_DMA(gsrc, ldst, NP) do { _Pragma("unroll") for (int _i = 0; _i < (NP); ++_i) \
;     __builtin_amdgcn_global_load_lds((const unsigned*)((gsrc) + _i * 1024), (LAS unsigned*)((ldst) + _i * 1024), 16, 0, 0); } while (0)
; DI void peer_token(LAS unsigned char* ring, const bf16* x1row, float inv2, const float* nffn, const int* ex, const float* pg, const unsigned char* U6, const unsigned char* V6,
;                    const float* usc, const float* vsc, float* orow, int lane) {
;     ...
;     const unsigned char* ul = U6 + lane * 16; const unsigned char* vl = V6 + lane * 16;
;     {
; #pragma unroll
;         for (int j = 0; j < 8; ++j) { const int ej = __builtin_amdgcn_readlane(e_lo, j); P11_DMA(ul + (size_t)ej * ROW4, ring + j * ROW4, 2); }
;     }
;     float cf_lo = 0.f, cf_hi = 0.f;
	v_lshl_add_u64 v[98:99], v[72:73], 0, s[46:47]
	v_readlane_b32 s46, v112, 1
	s_ashr_i32 s47, s46, 31
	global_load_lds_dwordx4 v[98:99], off
	v_lshl_add_u64 v[98:99], v[98:99], 0, s[72:73]
	s_mov_b32 m0, s85
	s_lshl_b64 s[46:47], s[46:47], 11
	global_load_lds_dwordx4 v[98:99], off
	v_lshl_add_u64 v[98:99], v[72:73], 0, s[46:47]
	s_add_i32 m0, s33, 0x800
	s_nop 0
	global_load_lds_dwordx4 v[98:99], off
	v_lshl_add_u64 v[98:99], v[98:99], 0, s[72:73]
	s_mov_b32 m0, s86
	s_movk_i32 s46, 0x800
	global_load_lds_dwordx4 v[98:99], off
	v_lshl_add_u64 v[98:99], v[72:73], 0, s[74:75]
	v_readlane_b32 s74, v112, 3
	s_add_i32 m0, s33, 0x1000
	s_ashr_i32 s75, s74, 31
	global_load_lds_dwordx4 v[98:99], off
	v_lshl_add_u64 v[98:99], v[98:99], 0, s[72:73]
	s_mov_b32 m0, s87
	s_lshl_b64 s[74:75], s[74:75], 11
	global_load_lds_dwordx4 v[98:99], off
	v_lshl_add_u64 v[98:99], v[72:73], 0, s[74:75]
	v_readlane_b32 s74, v112, 4
	s_mov_b32 m0, s88
	s_ashr_i32 s75, s74, 31
	global_load_lds_dwordx4 v[98:99], off
	v_lshl_add_u64 v[98:99], v[98:99], 0, s[72:73]
	s_mov_b32 m0, s89
	s_lshl_b64 s[74:75], s[74:75], 11
	global_load_lds_dwordx4 v[98:99], off
	v_lshl_add_u64 v[98:99], v[72:73], 0, s[74:75]
	v_readlane_b32 s74, v112, 5
	s_add_i32 m0, s33, 0x2000
	s_ashr_i32 s75, s74, 31
	global_load_lds_dwordx4 v[98:99], off
	v_lshl_add_u64 v[98:99], v[98:99], 0, s[72:73]
	s_mov_b32 m0, s90
	s_lshl_b64 s[74:75], s[74:75], 11
	global_load_lds_dwordx4 v[98:99], off
	v_lshl_add_u64 v[98:99], v[72:73], 0, s[74:75]
	v_readlane_b32 s74, v112, 6
	s_mov_b32 m0, s91
	s_ashr_i32 s75, s74, 31
	global_load_lds_dwordx4 v[98:99], off
	v_lshl_add_u64 v[98:99], v[98:99], 0, s[72:73]
	s_mov_b32 m0, s92
	s_lshl_b64 s[74:75], s[74:75], 11
	global_load_lds_dwordx4 v[98:99], off
	v_lshl_add_u64 v[98:99], v[72:73], 0, s[74:75]
	v_readlane_b32 s74, v112, 7
	s_add_i32 m0, s33, 0x3000
	s_ashr_i32 s75, s74, 31
	global_load_lds_dwordx4 v[98:99], off
	v_lshl_add_u64 v[98:99], v[98:99], 0, s[72:73]
	s_mov_b32 m0, s93
	s_lshl_b64 s[74:75], s[74:75], 11
	global_load_lds_dwordx4 v[98:99], off
	v_lshl_add_u64 v[98:99], v[72:73], 0, s[74:75]
	s_mov_b32 m0, s94
	s_nop 0
	global_load_lds_dwordx4 v[98:99], off
	v_lshl_add_u64 v[98:99], v[98:99], 0, s[72:73]
	s_mov_b32 m0, s95
	s_nop 0
	global_load_lds_dwordx4 v[98:99], off
	v_mul_f32_e32 v122, v123, v122
	s_mov_b32 s46, 0
	s_waitcnt vmcnt(14)
	v_add_u32_e32 v4, s33, v70
	ds_read_b128 v[98:101], v4
	ds_read_b128 v[102:105], v4 offset:1024
	v_readlane_b32 s78, v112, 8
	s_lshl_b32 s78, s78, 11
	s_mov_b32 s79, 0
	v_lshl_add_u64 v[2:3], v[72:73], 0, s[78:79]
	s_waitcnt lgkmcnt(0)
	s_mov_b32 m0, s33
	s_nop 0
	global_load_lds_dwordx4 v[2:3], off
	global_load_lds_dwordx4 v[2:3], off offset:1024
	s_add_i32 s47, s46, 1
	s_and_b32 s47, s47, 7
	s_lshl_b32 s47, s47, 11
	s_add_i32 s77, s33, s47
	v_add_u32_e32 v4, s77, v70
	s_add_i32 s78, s46, 9
	s_and_b32 s75, s78, 0x7f
	v_readlane_b32 s79, v113, s75
	v_readlane_b32 s47, v112, s75
	s_bitcmp1_b32 s75, 6
	s_cselect_b32 s47, s79, s47
	s_lshl_b32 s47, s47, 11
	s_bitcmp1_b32 s78, 7
	s_cselect_b32 s78, s98, 0
	s_cselect_b32 s79, s99, 0
	s_add_u32 s78, s78, s47
	s_addc_u32 s79, s79, 0
	s_waitcnt vmcnt(14)
	ds_read_b128 v[126:129], v4
	ds_read_b128 v[130:133], v4 offset:1024
	v_lshl_add_u64 v[2:3], v[72:73], 0, s[78:79]
	v_cvt_scalef32_pk_f32_fp4 v[136:137], v98, 1.0
	v_cvt_scalef32_pk_f32_fp4 v[138:139], v98, 1.0 op_sel:[1,0,0]
	v_cvt_scalef32_pk_f32_fp4 v[140:141], v98, 1.0 op_sel:[0,1,0]
	v_cvt_scalef32_pk_f32_fp4 v[142:143], v98, 1.0 op_sel:[1,1,0]
	v_pk_fma_f32 v[8:9], v[20:21], v[136:137], 0 op_sel_hi:[1,1,0]
	v_pk_fma_f32 v[10:11], v[22:23], v[138:139], 0 op_sel_hi:[1,1,0]
	v_pk_fma_f32 v[12:13], v[24:25], v[140:141], 0 op_sel_hi:[1,1,0]
	v_pk_fma_f32 v[14:15], v[26:27], v[142:143], 0 op_sel_hi:[1,1,0]
	v_cvt_scalef32_pk_f32_fp4 v[136:137], v99, 1.0
	v_cvt_scalef32_pk_f32_fp4 v[138:139], v99, 1.0 op_sel:[1,0,0]
	v_cvt_scalef32_pk_f32_fp4 v[140:141], v99, 1.0 op_sel:[0,1,0]
	v_cvt_scalef32_pk_f32_fp4 v[142:143], v99, 1.0 op_sel:[1,1,0]
	v_pk_fma_f32 v[8:9], v[28:29], v[136:137], v[8:9]
	v_pk_fma_f32 v[10:11], v[30:31], v[138:139], v[10:11]
	v_pk_fma_f32 v[12:13], v[32:33], v[140:141], v[12:13]
	v_pk_fma_f32 v[14:15], v[34:35], v[142:143], v[14:15]
	v_cvt_scalef32_pk_f32_fp4 v[136:137], v100, 1.0
	v_cvt_scalef32_pk_f32_fp4 v[138:139], v100, 1.0 op_sel:[1,0,0]
	v_cvt_scalef32_pk_f32_fp4 v[140:141], v100, 1.0 op_sel:[0,1,0]
	v_cvt_scalef32_pk_f32_fp4 v[142:143], v100, 1.0 op_sel:[1,1,0]
	v_pk_fma_f32 v[8:9], v[36:37], v[136:137], v[8:9]
	v_pk_fma_f32 v[10:11], v[38:39], v[138:139], v[10:11]
	v_pk_fma_f32 v[12:13], v[40:41], v[140:141], v[12:13]
	v_pk_fma_f32 v[14:15], v[42:43], v[142:143], v[14:15]
	s_waitcnt lgkmcnt(0)
	s_mov_b32 m0, s77
	s_nop 0
	global_load_lds_dwordx4 v[2:3], off
	global_load_lds_dwordx4 v[2:3], off offset:1024
	v_cvt_scalef32_pk_f32_fp4 v[136:137], v101, 1.0
	v_cvt_scalef32_pk_f32_fp4 v[138:139], v101, 1.0 op_sel:[1,0,0]
	v_cvt_scalef32_pk_f32_fp4 v[140:141], v101, 1.0 op_sel:[0,1,0]
	v_cvt_scalef32_pk_f32_fp4 v[142:143], v101, 1.0 op_sel:[1,1,0]
	v_pk_fma_f32 v[8:9], v[44:45], v[136:137], v[8:9]
	v_pk_fma_f32 v[10:11], v[46:47], v[138:139], v[10:11]
	v_pk_fma_f32 v[12:13], v[48:49], v[140:141], v[12:13]
	v_pk_fma_f32 v[14:15], v[50:51], v[142:143], v[14:15]
	v_cvt_scalef32_pk_f32_fp4 v[136:137], v102, 1.0
	v_cvt_scalef32_pk_f32_fp4 v[138:139], v102, 1.0 op_sel:[1,0,0]
	v_cvt_scalef32_pk_f32_fp4 v[140:141], v102, 1.0 op_sel:[0,1,0]
	v_cvt_scalef32_pk_f32_fp4 v[142:143], v102, 1.0 op_sel:[1,1,0]
	v_pk_fma_f32 v[8:9], v[52:53], v[136:137], v[8:9]
	v_pk_fma_f32 v[10:11], v[54:55], v[138:139], v[10:11]
	v_pk_fma_f32 v[12:13], v[56:57], v[140:141], v[12:13]
	v_pk_fma_f32 v[14:15], v[58:59], v[142:143], v[14:15]
	v_cvt_scalef32_pk_f32_fp4 v[136:137], v103, 1.0
	v_cvt_scalef32_pk_f32_fp4 v[138:139], v103, 1.0 op_sel:[1,0,0]
	v_cvt_scalef32_pk_f32_fp4 v[140:141], v103, 1.0 op_sel:[0,1,0]
	v_cvt_scalef32_pk_f32_fp4 v[142:143], v103, 1.0 op_sel:[1,1,0]
	v_pk_fma_f32 v[8:9], v[60:61], v[136:137], v[8:9]
	v_pk_fma_f32 v[10:11], v[62:63], v[138:139], v[10:11]
	v_pk_fma_f32 v[12:13], v[64:65], v[140:141], v[12:13]
	v_pk_fma_f32 v[14:15], v[80:81], v[142:143], v[14:15]
	v_cvt_scalef32_pk_f32_fp4 v[136:137], v104, 1.0
	v_cvt_scalef32_pk_f32_fp4 v[138:139], v104, 1.0 op_sel:[1,0,0]
	v_cvt_scalef32_pk_f32_fp4 v[140:141], v104, 1.0 op_sel:[0,1,0]
	v_cvt_scalef32_pk_f32_fp4 v[142:143], v104, 1.0 op_sel:[1,1,0]
	v_pk_fma_f32 v[8:9], v[82:83], v[136:137], v[8:9]
	v_pk_fma_f32 v[10:11], v[84:85], v[138:139], v[10:11]
	v_pk_fma_f32 v[12:13], v[86:87], v[140:141], v[12:13]
	v_pk_fma_f32 v[14:15], v[88:89], v[142:143], v[14:15]
	v_cvt_scalef32_pk_f32_fp4 v[136:137], v105, 1.0
	v_cvt_scalef32_pk_f32_fp4 v[138:139], v105, 1.0 op_sel:[1,0,0]
	v_cvt_scalef32_pk_f32_fp4 v[140:141], v105, 1.0 op_sel:[0,1,0]
	v_cvt_scalef32_pk_f32_fp4 v[142:143], v105, 1.0 op_sel:[1,1,0]
	v_pk_fma_f32 v[8:9], v[90:91], v[136:137], v[8:9]
	v_pk_fma_f32 v[10:11], v[92:93], v[138:139], v[10:11]
	v_pk_fma_f32 v[12:13], v[94:95], v[140:141], v[12:13]
	v_pk_fma_f32 v[14:15], v[96:97], v[142:143], v[14:15]
	v_pk_add_f32 v[8:9], v[8:9], v[10:11]
	v_pk_add_f32 v[12:13], v[12:13], v[14:15]
	v_pk_add_f32 v[8:9], v[8:9], v[12:13]
	v_add_f32_e32 v5, v8, v9
	s_mov_b32 s46, 1
.Lu_sweep_lo:
	s_add_i32 s47, s46, 1
	s_and_b32 s47, s47, 7
	s_lshl_b32 s47, s47, 11
	s_add_i32 s77, s33, s47
	v_add_u32_e32 v4, s77, v70
	s_add_i32 s78, s46, 9
	s_and_b32 s75, s78, 0x7f
	v_readlane_b32 s79, v113, s75
	v_readlane_b32 s47, v112, s75
	s_bitcmp1_b32 s75, 6
	s_cselect_b32 s47, s79, s47
	s_lshl_b32 s47, s47, 11
	s_bitcmp1_b32 s78, 7
	s_cselect_b32 s78, s98, 0
	s_cselect_b32 s79, s99, 0
	s_add_u32 s78, s78, s47
	s_addc_u32 s79, s79, 0
	s_add_i32 s32, s46, -1
	s_waitcnt vmcnt(14)
	ds_read_b128 v[98:101], v4
	ds_read_b128 v[102:105], v4 offset:1024
	v_lshl_add_u64 v[2:3], v[72:73], 0, s[78:79]
	v_cvt_scalef32_pk_f32_fp4 v[136:137], v126, 1.0
	v_cvt_scalef32_pk_f32_fp4 v[138:139], v126, 1.0 op_sel:[1,0,0]
	v_cvt_scalef32_pk_f32_fp4 v[140:141], v126, 1.0 op_sel:[0,1,0]
	v_cvt_scalef32_pk_f32_fp4 v[142:143], v126, 1.0 op_sel:[1,1,0]
	v_add_f32_dpp v5, v5, v5 quad_perm:[1,0,3,2] row_mask:0xf bank_mask:0xf bound_ctrl:1
	v_pk_fma_f32 v[8:9], v[20:21], v[136:137], 0 op_sel_hi:[1,1,0]
	v_pk_fma_f32 v[10:11], v[22:23], v[138:139], 0 op_sel_hi:[1,1,0]
	v_pk_fma_f32 v[12:13], v[24:25], v[140:141], 0 op_sel_hi:[1,1,0]
	v_pk_fma_f32 v[14:15], v[26:27], v[142:143], 0 op_sel_hi:[1,1,0]
	v_add_f32_dpp v5, v5, v5 quad_perm:[2,3,0,1] row_mask:0xf bank_mask:0xf bound_ctrl:1
	v_cvt_scalef32_pk_f32_fp4 v[136:137], v127, 1.0
	v_cvt_scalef32_pk_f32_fp4 v[138:139], v127, 1.0 op_sel:[1,0,0]
	v_cvt_scalef32_pk_f32_fp4 v[140:141], v127, 1.0 op_sel:[0,1,0]
	v_cvt_scalef32_pk_f32_fp4 v[142:143], v127, 1.0 op_sel:[1,1,0]
	v_add_f32_dpp v5, v5, v5 row_half_mirror row_mask:0xf bank_mask:0xf bound_ctrl:1
	v_pk_fma_f32 v[8:9], v[28:29], v[136:137], v[8:9]
	v_pk_fma_f32 v[10:11], v[30:31], v[138:139], v[10:11]
	v_pk_fma_f32 v[12:13], v[32:33], v[140:141], v[12:13]
	v_pk_fma_f32 v[14:15], v[34:35], v[142:143], v[14:15]
	v_mov_b32_e32 v7, 0
	v_cvt_scalef32_pk_f32_fp4 v[136:137], v128, 1.0
	v_cvt_scalef32_pk_f32_fp4 v[138:139], v128, 1.0 op_sel:[1,0,0]
	v_cvt_scalef32_pk_f32_fp4 v[140:141], v128, 1.0 op_sel:[0,1,0]
	v_cvt_scalef32_pk_f32_fp4 v[142:143], v128, 1.0 op_sel:[1,1,0]
	v_add_f32_dpp v5, v5, v5 row_mirror row_mask:0xf bank_mask:0xf bound_ctrl:1
	v_pk_fma_f32 v[8:9], v[36:37], v[136:137], v[8:9]
	v_pk_fma_f32 v[10:11], v[38:39], v[138:139], v[10:11]
	v_pk_fma_f32 v[12:13], v[40:41], v[140:141], v[12:13]
	v_pk_fma_f32 v[14:15], v[42:43], v[142:143], v[14:15]
	s_waitcnt lgkmcnt(0)
	s_mov_b32 m0, s77
	s_nop 0
	global_load_lds_dwordx4 v[2:3], off
	global_load_lds_dwordx4 v[2:3], off offset:1024
	v_cvt_scalef32_pk_f32_fp4 v[136:137], v129, 1.0
	v_cvt_scalef32_pk_f32_fp4 v[138:139], v129, 1.0 op_sel:[1,0,0]
	v_cvt_scalef32_pk_f32_fp4 v[140:141], v129, 1.0 op_sel:[0,1,0]
	v_cvt_scalef32_pk_f32_fp4 v[142:143], v129, 1.0 op_sel:[1,1,0]
	v_mov_b32_dpp v7, v5 row_bcast:15 row_mask:0xa bank_mask:0xf
	v_pk_fma_f32 v[8:9], v[44:45], v[136:137], v[8:9]
	v_pk_fma_f32 v[10:11], v[46:47], v[138:139], v[10:11]
	v_pk_fma_f32 v[12:13], v[48:49], v[140:141], v[12:13]
	v_pk_fma_f32 v[14:15], v[50:51], v[142:143], v[14:15]
	v_add_f32_e32 v5, v5, v7
	v_cvt_scalef32_pk_f32_fp4 v[136:137], v130, 1.0
	v_cvt_scalef32_pk_f32_fp4 v[138:139], v130, 1.0 op_sel:[1,0,0]
	v_cvt_scalef32_pk_f32_fp4 v[140:141], v130, 1.0 op_sel:[0,1,0]
	v_cvt_scalef32_pk_f32_fp4 v[142:143], v130, 1.0 op_sel:[1,1,0]
	v_mov_b32_e32 v7, 0
	v_pk_fma_f32 v[8:9], v[52:53], v[136:137], v[8:9]
	v_pk_fma_f32 v[10:11], v[54:55], v[138:139], v[10:11]
	v_pk_fma_f32 v[12:13], v[56:57], v[140:141], v[12:13]
	v_pk_fma_f32 v[14:15], v[58:59], v[142:143], v[14:15]
	v_mov_b32_dpp v7, v5 row_bcast:31 row_mask:0xc bank_mask:0xf
	v_cvt_scalef32_pk_f32_fp4 v[136:137], v131, 1.0
	v_cvt_scalef32_pk_f32_fp4 v[138:139], v131, 1.0 op_sel:[1,0,0]
	v_cvt_scalef32_pk_f32_fp4 v[140:141], v131, 1.0 op_sel:[0,1,0]
	v_cvt_scalef32_pk_f32_fp4 v[142:143], v131, 1.0 op_sel:[1,1,0]
	v_add_f32_e32 v5, v5, v7
	v_pk_fma_f32 v[8:9], v[60:61], v[136:137], v[8:9]
	v_pk_fma_f32 v[10:11], v[62:63], v[138:139], v[10:11]
	v_pk_fma_f32 v[12:13], v[64:65], v[140:141], v[12:13]
	v_pk_fma_f32 v[14:15], v[80:81], v[142:143], v[14:15]
	v_readlane_b32 s74, v5, 63
	v_cvt_scalef32_pk_f32_fp4 v[136:137], v132, 1.0
	v_cvt_scalef32_pk_f32_fp4 v[138:139], v132, 1.0 op_sel:[1,0,0]
	v_cvt_scalef32_pk_f32_fp4 v[140:141], v132, 1.0 op_sel:[0,1,0]
	v_cvt_scalef32_pk_f32_fp4 v[142:143], v132, 1.0 op_sel:[1,1,0]
	s_lshl_b64 exec, 1, s32
	v_mov_b32_e32 v120, s74
	s_mov_b64 exec, -1
	v_pk_fma_f32 v[8:9], v[82:83], v[136:137], v[8:9]
	v_pk_fma_f32 v[10:11], v[84:85], v[138:139], v[10:11]
	v_pk_fma_f32 v[12:13], v[86:87], v[140:141], v[12:13]
	v_pk_fma_f32 v[14:15], v[88:89], v[142:143], v[14:15]
	v_cvt_scalef32_pk_f32_fp4 v[136:137], v133, 1.0
	v_cvt_scalef32_pk_f32_fp4 v[138:139], v133, 1.0 op_sel:[1,0,0]
	v_cvt_scalef32_pk_f32_fp4 v[140:141], v133, 1.0 op_sel:[0,1,0]
	v_cvt_scalef32_pk_f32_fp4 v[142:143], v133, 1.0 op_sel:[1,1,0]
	v_pk_fma_f32 v[8:9], v[90:91], v[136:137], v[8:9]
	v_pk_fma_f32 v[10:11], v[92:93], v[138:139], v[10:11]
	v_pk_fma_f32 v[12:13], v[94:95], v[140:141], v[12:13]
	v_pk_fma_f32 v[14:15], v[96:97], v[142:143], v[14:15]
	v_pk_add_f32 v[8:9], v[8:9], v[10:11]
	v_pk_add_f32 v[12:13], v[12:13], v[14:15]
	v_pk_add_f32 v[8:9], v[8:9], v[12:13]
	v_add_f32_e32 v6, v8, v9
	s_add_i32 s47, s46, 2
	s_and_b32 s47, s47, 7
	s_lshl_b32 s47, s47, 11
	s_add_i32 s77, s33, s47
	v_add_u32_e32 v4, s77, v70
	s_add_i32 s78, s46, 10
	s_and_b32 s75, s78, 0x7f
	v_readlane_b32 s79, v113, s75
	v_readlane_b32 s47, v112, s75
	s_bitcmp1_b32 s75, 6
	s_cselect_b32 s47, s79, s47
	s_lshl_b32 s47, s47, 11
	s_bitcmp1_b32 s78, 7
	s_cselect_b32 s78, s98, 0
	s_cselect_b32 s79, s99, 0
	s_add_u32 s78, s78, s47
	s_addc_u32 s79, s79, 0
	s_add_i32 s32, s46, 0
	s_waitcnt vmcnt(14)
	ds_read_b128 v[126:129], v4
	ds_read_b128 v[130:133], v4 offset:1024
	v_lshl_add_u64 v[2:3], v[72:73], 0, s[78:79]
	v_cvt_scalef32_pk_f32_fp4 v[136:137], v98, 1.0
	v_cvt_scalef32_pk_f32_fp4 v[138:139], v98, 1.0 op_sel:[1,0,0]
	v_cvt_scalef32_pk_f32_fp4 v[140:141], v98, 1.0 op_sel:[0,1,0]
	v_cvt_scalef32_pk_f32_fp4 v[142:143], v98, 1.0 op_sel:[1,1,0]
	v_add_f32_dpp v6, v6, v6 quad_perm:[1,0,3,2] row_mask:0xf bank_mask:0xf bound_ctrl:1
	v_pk_fma_f32 v[8:9], v[20:21], v[136:137], 0 op_sel_hi:[1,1,0]
	v_pk_fma_f32 v[10:11], v[22:23], v[138:139], 0 op_sel_hi:[1,1,0]
	v_pk_fma_f32 v[12:13], v[24:25], v[140:141], 0 op_sel_hi:[1,1,0]
	v_pk_fma_f32 v[14:15], v[26:27], v[142:143], 0 op_sel_hi:[1,1,0]
	v_add_f32_dpp v6, v6, v6 quad_perm:[2,3,0,1] row_mask:0xf bank_mask:0xf bound_ctrl:1
	v_cvt_scalef32_pk_f32_fp4 v[136:137], v99, 1.0
	v_cvt_scalef32_pk_f32_fp4 v[138:139], v99, 1.0 op_sel:[1,0,0]
	v_cvt_scalef32_pk_f32_fp4 v[140:141], v99, 1.0 op_sel:[0,1,0]
	v_cvt_scalef32_pk_f32_fp4 v[142:143], v99, 1.0 op_sel:[1,1,0]
	v_add_f32_dpp v6, v6, v6 row_half_mirror row_mask:0xf bank_mask:0xf bound_ctrl:1
	v_pk_fma_f32 v[8:9], v[28:29], v[136:137], v[8:9]
	v_pk_fma_f32 v[10:11], v[30:31], v[138:139], v[10:11]
	v_pk_fma_f32 v[12:13], v[32:33], v[140:141], v[12:13]
	v_pk_fma_f32 v[14:15], v[34:35], v[142:143], v[14:15]
	v_mov_b32_e32 v7, 0
	v_cvt_scalef32_pk_f32_fp4 v[136:137], v100, 1.0
	v_cvt_scalef32_pk_f32_fp4 v[138:139], v100, 1.0 op_sel:[1,0,0]
	v_cvt_scalef32_pk_f32_fp4 v[140:141], v100, 1.0 op_sel:[0,1,0]
	v_cvt_scalef32_pk_f32_fp4 v[142:143], v100, 1.0 op_sel:[1,1,0]
	v_add_f32_dpp v6, v6, v6 row_mirror row_mask:0xf bank_mask:0xf bound_ctrl:1
	v_pk_fma_f32 v[8:9], v[36:37], v[136:137], v[8:9]
	v_pk_fma_f32 v[10:11], v[38:39], v[138:139], v[10:11]
	v_pk_fma_f32 v[12:13], v[40:41], v[140:141], v[12:13]
	v_pk_fma_f32 v[14:15], v[42:43], v[142:143], v[14:15]
	s_waitcnt lgkmcnt(0)
; DI void peer_token(LAS unsigned char* ring, const bf16* x1row, float inv2, const float* nffn, const int* ex, const float* pg, const unsigned char* U6, const unsigned char* V6,
;                    const float* usc, const float* vsc, float* orow, int lane) {
;     ...
; #pragma unroll 2
;     for (int k = 0; k < 56; ++k) P11_U(k, us_lo, gv_lo, cf_lo, ul, e_lo, k + 8);
; #pragma unroll 1
;     for (int k = 56; k < 64; ++k) P11_U(k, us_lo, gv_lo, cf_lo, ul, e_hi, k - 56);
; #pragma unroll 2
;     for (int k = 64; k < 120; ++k) P11_U(k, us_hi, gv_hi, cf_hi, ul, e_hi, k - 56);
	s_mov_b32 m0, s77
	s_nop 0
	global_load_lds_dwordx4 v[2:3], off
	global_load_lds_dwordx4 v[2:3], off offset:1024
	v_cvt_scalef32_pk_f32_fp4 v[136:137], v101, 1.0
	v_cvt_scalef32_pk_f32_fp4 v[138:139], v101, 1.0 op_sel:[1,0,0]
	v_cvt_scalef32_pk_f32_fp4 v[140:141], v101, 1.0 op_sel:[0,1,0]
	v_cvt_scalef32_pk_f32_fp4 v[142:143], v101, 1.0 op_sel:[1,1,0]
	v_mov_b32_dpp v7, v6 row_bcast:15 row_mask:0xa bank_mask:0xf
	v_pk_fma_f32 v[8:9], v[44:45], v[136:137], v[8:9]
	v_pk_fma_f32 v[10:11], v[46:47], v[138:139], v[10:11]
	v_pk_fma_f32 v[12:13], v[48:49], v[140:141], v[12:13]
	v_pk_fma_f32 v[14:15], v[50:51], v[142:143], v[14:15]
	v_add_f32_e32 v6, v6, v7
	v_cvt_scalef32_pk_f32_fp4 v[136:137], v102, 1.0
	v_cvt_scalef32_pk_f32_fp4 v[138:139], v102, 1.0 op_sel:[1,0,0]
	v_cvt_scalef32_pk_f32_fp4 v[140:141], v102, 1.0 op_sel:[0,1,0]
	v_cvt_scalef32_pk_f32_fp4 v[142:143], v102, 1.0 op_sel:[1,1,0]
	v_mov_b32_e32 v7, 0
	v_pk_fma_f32 v[8:9], v[52:53], v[136:137], v[8:9]
	v_pk_fma_f32 v[10:11], v[54:55], v[138:139], v[10:11]
	v_pk_fma_f32 v[12:13], v[56:57], v[140:141], v[12:13]
	v_pk_fma_f32 v[14:15], v[58:59], v[142:143], v[14:15]
	v_mov_b32_dpp v7, v6 row_bcast:31 row_mask:0xc bank_mask:0xf
	v_cvt_scalef32_pk_f32_fp4 v[136:137], v103, 1.0
	v_cvt_scalef32_pk_f32_fp4 v[138:139], v103, 1.0 op_sel:[1,0,0]
	v_cvt_scalef32_pk_f32_fp4 v[140:141], v103, 1.0 op_sel:[0,1,0]
	v_cvt_scalef32_pk_f32_fp4 v[142:143], v103, 1.0 op_sel:[1,1,0]
	v_add_f32_e32 v6, v6, v7
	v_pk_fma_f32 v[8:9], v[60:61], v[136:137], v[8:9]
	v_pk_fma_f32 v[10:11], v[62:63], v[138:139], v[10:11]
	v_pk_fma_f32 v[12:13], v[64:65], v[140:141], v[12:13]
	v_pk_fma_f32 v[14:15], v[80:81], v[142:143], v[14:15]
	v_readlane_b32 s74, v6, 63
	v_cvt_scalef32_pk_f32_fp4 v[136:137], v104, 1.0
	v_cvt_scalef32_pk_f32_fp4 v[138:139], v104, 1.0 op_sel:[1,0,0]
	v_cvt_scalef32_pk_f32_fp4 v[140:141], v104, 1.0 op_sel:[0,1,0]
	v_cvt_scalef32_pk_f32_fp4 v[142:143], v104, 1.0 op_sel:[1,1,0]
	s_lshl_b64 exec, 1, s32
	v_mov_b32_e32 v120, s74
	s_mov_b64 exec, -1
	v_pk_fma_f32 v[8:9], v[82:83], v[136:137], v[8:9]
	v_pk_fma_f32 v[10:11], v[84:85], v[138:139], v[10:11]
	v_pk_fma_f32 v[12:13], v[86:87], v[140:141], v[12:13]
	v_pk_fma_f32 v[14:15], v[88:89], v[142:143], v[14:15]
	v_cvt_scalef32_pk_f32_fp4 v[136:137], v105, 1.0
	v_cvt_scalef32_pk_f32_fp4 v[138:139], v105, 1.0 op_sel:[1,0,0]
	v_cvt_scalef32_pk_f32_fp4 v[140:141], v105, 1.0 op_sel:[0,1,0]
	v_cvt_scalef32_pk_f32_fp4 v[142:143], v105, 1.0 op_sel:[1,1,0]
	v_pk_fma_f32 v[8:9], v[90:91], v[136:137], v[8:9]
	v_pk_fma_f32 v[10:11], v[92:93], v[138:139], v[10:11]
	v_pk_fma_f32 v[12:13], v[94:95], v[140:141], v[12:13]
	v_pk_fma_f32 v[14:15], v[96:97], v[142:143], v[14:15]
	v_pk_add_f32 v[8:9], v[8:9], v[10:11]
	v_pk_add_f32 v[12:13], v[12:13], v[14:15]
	v_pk_add_f32 v[8:9], v[8:9], v[12:13]
	v_add_f32_e32 v5, v8, v9
	s_add_i32 s46, s46, 2
	s_cmp_lg_u32 s46, 65
	s_cbranch_scc1 .Lu_sweep_lo
.Lu_sweep_hi:
	s_add_i32 s47, s46, 1
	s_and_b32 s47, s47, 7
	s_lshl_b32 s47, s47, 11
	s_add_i32 s77, s33, s47
	v_add_u32_e32 v4, s77, v70
	s_add_i32 s78, s46, 9
	s_and_b32 s75, s78, 0x7f
	v_readlane_b32 s79, v113, s75
	v_readlane_b32 s47, v112, s75
	s_bitcmp1_b32 s75, 6
	s_cselect_b32 s47, s79, s47
	s_lshl_b32 s47, s47, 11
	s_bitcmp1_b32 s78, 7
	s_cselect_b32 s78, s98, 0
	s_cselect_b32 s79, s99, 0
	s_add_u32 s78, s78, s47
	s_addc_u32 s79, s79, 0
	s_add_i32 s32, s46, -1
	s_waitcnt vmcnt(14)
	ds_read_b128 v[98:101], v4
	ds_read_b128 v[102:105], v4 offset:1024
	v_lshl_add_u64 v[2:3], v[72:73], 0, s[78:79]
	v_cvt_scalef32_pk_f32_fp4 v[136:137], v126, 1.0
	v_cvt_scalef32_pk_f32_fp4 v[138:139], v126, 1.0 op_sel:[1,0,0]
	v_cvt_scalef32_pk_f32_fp4 v[140:141], v126, 1.0 op_sel:[0,1,0]
	v_cvt_scalef32_pk_f32_fp4 v[142:143], v126, 1.0 op_sel:[1,1,0]
	v_add_f32_dpp v5, v5, v5 quad_perm:[1,0,3,2] row_mask:0xf bank_mask:0xf bound_ctrl:1
	v_pk_fma_f32 v[8:9], v[20:21], v[136:137], 0 op_sel_hi:[1,1,0]
	v_pk_fma_f32 v[10:11], v[22:23], v[138:139], 0 op_sel_hi:[1,1,0]
	v_pk_fma_f32 v[12:13], v[24:25], v[140:141], 0 op_sel_hi:[1,1,0]
	v_pk_fma_f32 v[14:15], v[26:27], v[142:143], 0 op_sel_hi:[1,1,0]
	v_add_f32_dpp v5, v5, v5 quad_perm:[2,3,0,1] row_mask:0xf bank_mask:0xf bound_ctrl:1
	v_cvt_scalef32_pk_f32_fp4 v[136:137], v127, 1.0
	v_cvt_scalef32_pk_f32_fp4 v[138:139], v127, 1.0 op_sel:[1,0,0]
	v_cvt_scalef32_pk_f32_fp4 v[140:141], v127, 1.0 op_sel:[0,1,0]
	v_cvt_scalef32_pk_f32_fp4 v[142:143], v127, 1.0 op_sel:[1,1,0]
	v_add_f32_dpp v5, v5, v5 row_half_mirror row_mask:0xf bank_mask:0xf bound_ctrl:1
	v_pk_fma_f32 v[8:9], v[28:29], v[136:137], v[8:9]
	v_pk_fma_f32 v[10:11], v[30:31], v[138:139], v[10:11]
	v_pk_fma_f32 v[12:13], v[32:33], v[140:141], v[12:13]
	v_pk_fma_f32 v[14:15], v[34:35], v[142:143], v[14:15]
	v_mov_b32_e32 v7, 0
	v_cvt_scalef32_pk_f32_fp4 v[136:137], v128, 1.0
	v_cvt_scalef32_pk_f32_fp4 v[138:139], v128, 1.0 op_sel:[1,0,0]
	v_cvt_scalef32_pk_f32_fp4 v[140:141], v128, 1.0 op_sel:[0,1,0]
	v_cvt_scalef32_pk_f32_fp4 v[142:143], v128, 1.0 op_sel:[1,1,0]
	v_add_f32_dpp v5, v5, v5 row_mirror row_mask:0xf bank_mask:0xf bound_ctrl:1
	v_pk_fma_f32 v[8:9], v[36:37], v[136:137], v[8:9]
	v_pk_fma_f32 v[10:11], v[38:39], v[138:139], v[10:11]
	v_pk_fma_f32 v[12:13], v[40:41], v[140:141], v[12:13]
	v_pk_fma_f32 v[14:15], v[42:43], v[142:143], v[14:15]
	s_waitcnt lgkmcnt(0)
; DI void peer_token(LAS unsigned char* ring, const bf16* x1row, float inv2, const float* nffn, const int* ex, const float* pg, const unsigned char* U6, const unsigned char* V6,
;                    const float* usc, const float* vsc, float* orow, int lane) {
;     ...
; #pragma unroll 2
;     for (int k = 0; k < 56; ++k) P11_U(k, us_lo, gv_lo, cf_lo, ul, e_lo, k + 8);
; #pragma unroll 1
;     for (int k = 56; k < 64; ++k) P11_U(k, us_lo, gv_lo, cf_lo, ul, e_hi, k - 56);
; #pragma unroll 2
;     for (int k = 64; k < 120; ++k) P11_U(k, us_hi, gv_hi, cf_hi, ul, e_hi, k - 56);
	s_mov_b32 m0, s77
	s_nop 0
	global_load_lds_dwordx4 v[2:3], off
	global_load_lds_dwordx4 v[2:3], off offset:1024
	v_cvt_scalef32_pk_f32_fp4 v[136:137], v129, 1.0
	v_cvt_scalef32_pk_f32_fp4 v[138:139], v129, 1.0 op_sel:[1,0,0]
	v_cvt_scalef32_pk_f32_fp4 v[140:141], v129, 1.0 op_sel:[0,1,0]
	v_cvt_scalef32_pk_f32_fp4 v[142:143], v129, 1.0 op_sel:[1,1,0]
	v_mov_b32_dpp v7, v5 row_bcast:15 row_mask:0xa bank_mask:0xf
	v_pk_fma_f32 v[8:9], v[44:45], v[136:137], v[8:9]
	v_pk_fma_f32 v[10:11], v[46:47], v[138:139], v[10:11]
	v_pk_fma_f32 v[12:13], v[48:49], v[140:141], v[12:13]
	v_pk_fma_f32 v[14:15], v[50:51], v[142:143], v[14:15]
	v_add_f32_e32 v5, v5, v7
	v_cvt_scalef32_pk_f32_fp4 v[136:137], v130, 1.0
	v_cvt_scalef32_pk_f32_fp4 v[138:139], v130, 1.0 op_sel:[1,0,0]
	v_cvt_scalef32_pk_f32_fp4 v[140:141], v130, 1.0 op_sel:[0,1,0]
	v_cvt_scalef32_pk_f32_fp4 v[142:143], v130, 1.0 op_sel:[1,1,0]
	v_mov_b32_e32 v7, 0
	v_pk_fma_f32 v[8:9], v[52:53], v[136:137], v[8:9]
	v_pk_fma_f32 v[10:11], v[54:55], v[138:139], v[10:11]
	v_pk_fma_f32 v[12:13], v[56:57], v[140:141], v[12:13]
	v_pk_fma_f32 v[14:15], v[58:59], v[142:143], v[14:15]
	v_mov_b32_dpp v7, v5 row_bcast:31 row_mask:0xc bank_mask:0xf
	v_cvt_scalef32_pk_f32_fp4 v[136:137], v131, 1.0
	v_cvt_scalef32_pk_f32_fp4 v[138:139], v131, 1.0 op_sel:[1,0,0]
	v_cvt_scalef32_pk_f32_fp4 v[140:141], v131, 1.0 op_sel:[0,1,0]
	v_cvt_scalef32_pk_f32_fp4 v[142:143], v131, 1.0 op_sel:[1,1,0]
	v_add_f32_e32 v5, v5, v7
	v_pk_fma_f32 v[8:9], v[60:61], v[136:137], v[8:9]
	v_pk_fma_f32 v[10:11], v[62:63], v[138:139], v[10:11]
	v_pk_fma_f32 v[12:13], v[64:65], v[140:141], v[12:13]
	v_pk_fma_f32 v[14:15], v[80:81], v[142:143], v[14:15]
	v_readlane_b32 s74, v5, 63
	v_cvt_scalef32_pk_f32_fp4 v[136:137], v132, 1.0
	v_cvt_scalef32_pk_f32_fp4 v[138:139], v132, 1.0 op_sel:[1,0,0]
	v_cvt_scalef32_pk_f32_fp4 v[140:141], v132, 1.0 op_sel:[0,1,0]
	v_cvt_scalef32_pk_f32_fp4 v[142:143], v132, 1.0 op_sel:[1,1,0]
	s_lshl_b64 exec, 1, s32
	v_mov_b32_e32 v125, s74
	s_mov_b64 exec, -1
	v_pk_fma_f32 v[8:9], v[82:83], v[136:137], v[8:9]
	v_pk_fma_f32 v[10:11], v[84:85], v[138:139], v[10:11]
	v_pk_fma_f32 v[12:13], v[86:87], v[140:141], v[12:13]
	v_pk_fma_f32 v[14:15], v[88:89], v[142:143], v[14:15]
	v_cvt_scalef32_pk_f32_fp4 v[136:137], v133, 1.0
	v_cvt_scalef32_pk_f32_fp4 v[138:139], v133, 1.0 op_sel:[1,0,0]
	v_cvt_scalef32_pk_f32_fp4 v[140:141], v133, 1.0 op_sel:[0,1,0]
	v_cvt_scalef32_pk_f32_fp4 v[142:143], v133, 1.0 op_sel:[1,1,0]
	v_pk_fma_f32 v[8:9], v[90:91], v[136:137], v[8:9]
	v_pk_fma_f32 v[10:11], v[92:93], v[138:139], v[10:11]
	v_pk_fma_f32 v[12:13], v[94:95], v[140:141], v[12:13]
	v_pk_fma_f32 v[14:15], v[96:97], v[142:143], v[14:15]
	v_pk_add_f32 v[8:9], v[8:9], v[10:11]
	v_pk_add_f32 v[12:13], v[12:13], v[14:15]
	v_pk_add_f32 v[8:9], v[8:9], v[12:13]
	v_add_f32_e32 v6, v8, v9
	s_add_i32 s47, s46, 2
	s_and_b32 s47, s47, 7
	s_lshl_b32 s47, s47, 11
	s_add_i32 s77, s33, s47
	v_add_u32_e32 v4, s77, v70
	s_add_i32 s78, s46, 10
	s_and_b32 s75, s78, 0x7f
	v_readlane_b32 s79, v113, s75
	v_readlane_b32 s47, v112, s75
	s_bitcmp1_b32 s75, 6
	s_cselect_b32 s47, s79, s47
	s_lshl_b32 s47, s47, 11
	s_bitcmp1_b32 s78, 7
	s_cselect_b32 s78, s98, 0
	s_cselect_b32 s79, s99, 0
	s_add_u32 s78, s78, s47
	s_addc_u32 s79, s79, 0
	s_add_i32 s32, s46, 0
	s_waitcnt vmcnt(14)
	ds_read_b128 v[126:129], v4
	ds_read_b128 v[130:133], v4 offset:1024
	v_lshl_add_u64 v[2:3], v[72:73], 0, s[78:79]
	v_cvt_scalef32_pk_f32_fp4 v[136:137], v98, 1.0
	v_cvt_scalef32_pk_f32_fp4 v[138:139], v98, 1.0 op_sel:[1,0,0]
	v_cvt_scalef32_pk_f32_fp4 v[140:141], v98, 1.0 op_sel:[0,1,0]
	v_cvt_scalef32_pk_f32_fp4 v[142:143], v98, 1.0 op_sel:[1,1,0]
	v_add_f32_dpp v6, v6, v6 quad_perm:[1,0,3,2] row_mask:0xf bank_mask:0xf bound_ctrl:1
	v_pk_fma_f32 v[8:9], v[20:21], v[136:137], 0 op_sel_hi:[1,1,0]
	v_pk_fma_f32 v[10:11], v[22:23], v[138:139], 0 op_sel_hi:[1,1,0]
	v_pk_fma_f32 v[12:13], v[24:25], v[140:141], 0 op_sel_hi:[1,1,0]
	v_pk_fma_f32 v[14:15], v[26:27], v[142:143], 0 op_sel_hi:[1,1,0]
	v_add_f32_dpp v6, v6, v6 quad_perm:[2,3,0,1] row_mask:0xf bank_mask:0xf bound_ctrl:1
	v_cvt_scalef32_pk_f32_fp4 v[136:137], v99, 1.0
	v_cvt_scalef32_pk_f32_fp4 v[138:139], v99, 1.0 op_sel:[1,0,0]
	v_cvt_scalef32_pk_f32_fp4 v[140:141], v99, 1.0 op_sel:[0,1,0]
	v_cvt_scalef32_pk_f32_fp4 v[142:143], v99, 1.0 op_sel:[1,1,0]
	v_add_f32_dpp v6, v6, v6 row_half_mirror row_mask:0xf bank_mask:0xf bound_ctrl:1
	v_pk_fma_f32 v[8:9], v[28:29], v[136:137], v[8:9]
	v_pk_fma_f32 v[10:11], v[30:31], v[138:139], v[10:11]
	v_pk_fma_f32 v[12:13], v[32:33], v[140:141], v[12:13]
	v_pk_fma_f32 v[14:15], v[34:35], v[142:143], v[14:15]
	v_mov_b32_e32 v7, 0
	v_cvt_scalef32_pk_f32_fp4 v[136:137], v100, 1.0
	v_cvt_scalef32_pk_f32_fp4 v[138:139], v100, 1.0 op_sel:[1,0,0]
	v_cvt_scalef32_pk_f32_fp4 v[140:141], v100, 1.0 op_sel:[0,1,0]
	v_cvt_scalef32_pk_f32_fp4 v[142:143], v100, 1.0 op_sel:[1,1,0]
	v_add_f32_dpp v6, v6, v6 row_mirror row_mask:0xf bank_mask:0xf bound_ctrl:1
	v_pk_fma_f32 v[8:9], v[36:37], v[136:137], v[8:9]
	v_pk_fma_f32 v[10:11], v[38:39], v[138:139], v[10:11]
	v_pk_fma_f32 v[12:13], v[40:41], v[140:141], v[12:13]
	v_pk_fma_f32 v[14:15], v[42:43], v[142:143], v[14:15]
	s_waitcnt lgkmcnt(0)
; DI void peer_token(LAS unsigned char* ring, const bf16* x1row, float inv2, const float* nffn, const int* ex, const float* pg, const unsigned char* U6, const unsigned char* V6,
;                    const float* usc, const float* vsc, float* orow, int lane) {
;     ...
; #pragma unroll 2
;     for (int k = 0; k < 56; ++k) P11_U(k, us_lo, gv_lo, cf_lo, ul, e_lo, k + 8);
; #pragma unroll 1
;     for (int k = 56; k < 64; ++k) P11_U(k, us_lo, gv_lo, cf_lo, ul, e_hi, k - 56);
; #pragma unroll 2
;     for (int k = 64; k < 120; ++k) P11_U(k, us_hi, gv_hi, cf_hi, ul, e_hi, k - 56);
; #pragma unroll 1
;     for (int k = 120; k < 128; ++k) P11_U(k, us_hi, gv_hi, cf_hi, vl, e_lo, k - 120);
	s_mov_b32 m0, s77
	s_nop 0
	global_load_lds_dwordx4 v[2:3], off
	global_load_lds_dwordx4 v[2:3], off offset:1024
	v_cvt_scalef32_pk_f32_fp4 v[136:137], v101, 1.0
	v_cvt_scalef32_pk_f32_fp4 v[138:139], v101, 1.0 op_sel:[1,0,0]
	v_cvt_scalef32_pk_f32_fp4 v[140:141], v101, 1.0 op_sel:[0,1,0]
	v_cvt_scalef32_pk_f32_fp4 v[142:143], v101, 1.0 op_sel:[1,1,0]
	v_mov_b32_dpp v7, v6 row_bcast:15 row_mask:0xa bank_mask:0xf
	v_pk_fma_f32 v[8:9], v[44:45], v[136:137], v[8:9]
	v_pk_fma_f32 v[10:11], v[46:47], v[138:139], v[10:11]
	v_pk_fma_f32 v[12:13], v[48:49], v[140:141], v[12:13]
	v_pk_fma_f32 v[14:15], v[50:51], v[142:143], v[14:15]
	v_add_f32_e32 v6, v6, v7
	v_cvt_scalef32_pk_f32_fp4 v[136:137], v102, 1.0
	v_cvt_scalef32_pk_f32_fp4 v[138:139], v102, 1.0 op_sel:[1,0,0]
	v_cvt_scalef32_pk_f32_fp4 v[140:141], v102, 1.0 op_sel:[0,1,0]
	v_cvt_scalef32_pk_f32_fp4 v[142:143], v102, 1.0 op_sel:[1,1,0]
	v_mov_b32_e32 v7, 0
	v_pk_fma_f32 v[8:9], v[52:53], v[136:137], v[8:9]
	v_pk_fma_f32 v[10:11], v[54:55], v[138:139], v[10:11]
	v_pk_fma_f32 v[12:13], v[56:57], v[140:141], v[12:13]
	v_pk_fma_f32 v[14:15], v[58:59], v[142:143], v[14:15]
	v_mov_b32_dpp v7, v6 row_bcast:31 row_mask:0xc bank_mask:0xf
	v_cvt_scalef32_pk_f32_fp4 v[136:137], v103, 1.0
	v_cvt_scalef32_pk_f32_fp4 v[138:139], v103, 1.0 op_sel:[1,0,0]
	v_cvt_scalef32_pk_f32_fp4 v[140:141], v103, 1.0 op_sel:[0,1,0]
	v_cvt_scalef32_pk_f32_fp4 v[142:143], v103, 1.0 op_sel:[1,1,0]
	v_add_f32_e32 v6, v6, v7
	v_pk_fma_f32 v[8:9], v[60:61], v[136:137], v[8:9]
	v_pk_fma_f32 v[10:11], v[62:63], v[138:139], v[10:11]
	v_pk_fma_f32 v[12:13], v[64:65], v[140:141], v[12:13]
	v_pk_fma_f32 v[14:15], v[80:81], v[142:143], v[14:15]
	v_readlane_b32 s74, v6, 63
	v_cvt_scalef32_pk_f32_fp4 v[136:137], v104, 1.0
	v_cvt_scalef32_pk_f32_fp4 v[138:139], v104, 1.0 op_sel:[1,0,0]
	v_cvt_scalef32_pk_f32_fp4 v[140:141], v104, 1.0 op_sel:[0,1,0]
	v_cvt_scalef32_pk_f32_fp4 v[142:143], v104, 1.0 op_sel:[1,1,0]
	s_lshl_b64 exec, 1, s32
	v_mov_b32_e32 v125, s74
	s_mov_b64 exec, -1
	v_pk_fma_f32 v[8:9], v[82:83], v[136:137], v[8:9]
	v_pk_fma_f32 v[10:11], v[84:85], v[138:139], v[10:11]
	v_pk_fma_f32 v[12:13], v[86:87], v[140:141], v[12:13]
	v_pk_fma_f32 v[14:15], v[88:89], v[142:143], v[14:15]
	v_cvt_scalef32_pk_f32_fp4 v[136:137], v105, 1.0
	v_cvt_scalef32_pk_f32_fp4 v[138:139], v105, 1.0 op_sel:[1,0,0]
	v_cvt_scalef32_pk_f32_fp4 v[140:141], v105, 1.0 op_sel:[0,1,0]
	v_cvt_scalef32_pk_f32_fp4 v[142:143], v105, 1.0 op_sel:[1,1,0]
	v_pk_fma_f32 v[8:9], v[90:91], v[136:137], v[8:9]
	v_pk_fma_f32 v[10:11], v[92:93], v[138:139], v[10:11]
	v_pk_fma_f32 v[12:13], v[94:95], v[140:141], v[12:13]
	v_pk_fma_f32 v[14:15], v[96:97], v[142:143], v[14:15]
	v_pk_add_f32 v[8:9], v[8:9], v[10:11]
	v_pk_add_f32 v[12:13], v[12:13], v[14:15]
	v_pk_add_f32 v[8:9], v[8:9], v[12:13]
	v_add_f32_e32 v5, v8, v9
	s_add_i32 s46, s46, 2
	s_cmp_lg_u32 s46, 127
	s_cbranch_scc1 .Lu_sweep_hi
	s_add_i32 s47, s46, 1
	s_and_b32 s47, s47, 7
	s_lshl_b32 s47, s47, 11
	s_add_i32 s77, s33, s47
	v_add_u32_e32 v4, s77, v70
	s_add_i32 s78, s46, 9
	s_and_b32 s75, s78, 0x7f
	v_readlane_b32 s79, v113, s75
	v_readlane_b32 s47, v112, s75
	s_bitcmp1_b32 s75, 6
	s_cselect_b32 s47, s79, s47
	s_lshl_b32 s47, s47, 11
	s_bitcmp1_b32 s78, 7
	s_cselect_b32 s78, s98, 0
	s_cselect_b32 s79, s99, 0
	s_add_u32 s78, s78, s47
	s_addc_u32 s79, s79, 0
	s_add_i32 s32, s46, -1
	s_waitcnt vmcnt(14)
	ds_read_b128 v[98:101], v4
	ds_read_b128 v[102:105], v4 offset:1024
	v_lshl_add_u64 v[2:3], v[72:73], 0, s[78:79]
	v_cvt_scalef32_pk_f32_fp4 v[136:137], v126, 1.0
	v_cvt_scalef32_pk_f32_fp4 v[138:139], v126, 1.0 op_sel:[1,0,0]
	v_cvt_scalef32_pk_f32_fp4 v[140:141], v126, 1.0 op_sel:[0,1,0]
	v_cvt_scalef32_pk_f32_fp4 v[142:143], v126, 1.0 op_sel:[1,1,0]
	v_add_f32_dpp v5, v5, v5 quad_perm:[1,0,3,2] row_mask:0xf bank_mask:0xf bound_ctrl:1
	v_pk_fma_f32 v[8:9], v[20:21], v[136:137], 0 op_sel_hi:[1,1,0]
	v_pk_fma_f32 v[10:11], v[22:23], v[138:139], 0 op_sel_hi:[1,1,0]
	v_pk_fma_f32 v[12:13], v[24:25], v[140:141], 0 op_sel_hi:[1,1,0]
	v_pk_fma_f32 v[14:15], v[26:27], v[142:143], 0 op_sel_hi:[1,1,0]
	v_add_f32_dpp v5, v5, v5 quad_perm:[2,3,0,1] row_mask:0xf bank_mask:0xf bound_ctrl:1
	v_cvt_scalef32_pk_f32_fp4 v[136:137], v127, 1.0
	v_cvt_scalef32_pk_f32_fp4 v[138:139], v127, 1.0 op_sel:[1,0,0]
	v_cvt_scalef32_pk_f32_fp4 v[140:141], v127, 1.0 op_sel:[0,1,0]
	v_cvt_scalef32_pk_f32_fp4 v[142:143], v127, 1.0 op_sel:[1,1,0]
	v_add_f32_dpp v5, v5, v5 row_half_mirror row_mask:0xf bank_mask:0xf bound_ctrl:1
	v_pk_fma_f32 v[8:9], v[28:29], v[136:137], v[8:9]
	v_pk_fma_f32 v[10:11], v[30:31], v[138:139], v[10:11]
	v_pk_fma_f32 v[12:13], v[32:33], v[140:141], v[12:13]
	v_pk_fma_f32 v[14:15], v[34:35], v[142:143], v[14:15]
	v_mov_b32_e32 v7, 0
	v_cvt_scalef32_pk_f32_fp4 v[136:137], v128, 1.0
	v_cvt_scalef32_pk_f32_fp4 v[138:139], v128, 1.0 op_sel:[1,0,0]
	v_cvt_scalef32_pk_f32_fp4 v[140:141], v128, 1.0 op_sel:[0,1,0]
	v_cvt_scalef32_pk_f32_fp4 v[142:143], v128, 1.0 op_sel:[1,1,0]
	v_add_f32_dpp v5, v5, v5 row_mirror row_mask:0xf bank_mask:0xf bound_ctrl:1
	v_pk_fma_f32 v[8:9], v[36:37], v[136:137], v[8:9]
	v_pk_fma_f32 v[10:11], v[38:39], v[138:139], v[10:11]
	v_pk_fma_f32 v[12:13], v[40:41], v[140:141], v[12:13]
	v_pk_fma_f32 v[14:15], v[42:43], v[142:143], v[14:15]
	s_waitcnt lgkmcnt(0)
; DI float gelu_exact(float v) {
;     const float av = fabsf(v), t = __builtin_amdgcn_rcpf(av * 0.2316418882f + 1.0f);
;     float q = t * 0.5307027145f + (-0.7265760135f); q = q * t + 0.7107068705f; q = q * t + (-0.142248368f); q = q * t + 0.127414796f; q = q * t;
;     const float e = __builtin_amdgcn_exp2f((v * v) * (-0.72134752044f));
;     const float m = v * (q * e);
;     return v < 0.f ? m : v - m;
; }
; DI void peer_token(LAS unsigned char* ring, const bf16* x1row, float inv2, const float* nffn, const int* ex, const float* pg, const unsigned char* U6, const unsigned char* V6,
;                    const float* usc, const float* vsc, float* orow, int lane) {
;     ...
; #pragma unroll 2
;     for (int k = 0; k < 56; ++k) P11_U(k, us_lo, gv_lo, cf_lo, ul, e_lo, k + 8);
; #pragma unroll 1
;     for (int k = 56; k < 64; ++k) P11_U(k, us_lo, gv_lo, cf_lo, ul, e_hi, k - 56);
; #pragma unroll 2
;     for (int k = 64; k < 120; ++k) P11_U(k, us_hi, gv_hi, cf_hi, ul, e_hi, k - 56);
; #pragma unroll 1
;     for (int k = 120; k < 128; ++k) P11_U(k, us_hi, gv_hi, cf_hi, vl, e_lo, k - 120);
	s_mov_b32 m0, s77
	s_nop 0
	global_load_lds_dwordx4 v[2:3], off
	global_load_lds_dwordx4 v[2:3], off offset:1024
	v_cvt_scalef32_pk_f32_fp4 v[136:137], v129, 1.0
	v_cvt_scalef32_pk_f32_fp4 v[138:139], v129, 1.0 op_sel:[1,0,0]
	v_cvt_scalef32_pk_f32_fp4 v[140:141], v129, 1.0 op_sel:[0,1,0]
	v_cvt_scalef32_pk_f32_fp4 v[142:143], v129, 1.0 op_sel:[1,1,0]
	v_mov_b32_dpp v7, v5 row_bcast:15 row_mask:0xa bank_mask:0xf
	v_pk_fma_f32 v[8:9], v[44:45], v[136:137], v[8:9]
	v_pk_fma_f32 v[10:11], v[46:47], v[138:139], v[10:11]
	v_pk_fma_f32 v[12:13], v[48:49], v[140:141], v[12:13]
	v_pk_fma_f32 v[14:15], v[50:51], v[142:143], v[14:15]
	v_add_f32_e32 v5, v5, v7
	v_cvt_scalef32_pk_f32_fp4 v[136:137], v130, 1.0
	v_cvt_scalef32_pk_f32_fp4 v[138:139], v130, 1.0 op_sel:[1,0,0]
	v_cvt_scalef32_pk_f32_fp4 v[140:141], v130, 1.0 op_sel:[0,1,0]
	v_cvt_scalef32_pk_f32_fp4 v[142:143], v130, 1.0 op_sel:[1,1,0]
	v_mov_b32_e32 v7, 0
	v_pk_fma_f32 v[8:9], v[52:53], v[136:137], v[8:9]
	v_pk_fma_f32 v[10:11], v[54:55], v[138:139], v[10:11]
	v_pk_fma_f32 v[12:13], v[56:57], v[140:141], v[12:13]
	v_pk_fma_f32 v[14:15], v[58:59], v[142:143], v[14:15]
	v_mov_b32_dpp v7, v5 row_bcast:31 row_mask:0xc bank_mask:0xf
	v_cvt_scalef32_pk_f32_fp4 v[136:137], v131, 1.0
	v_cvt_scalef32_pk_f32_fp4 v[138:139], v131, 1.0 op_sel:[1,0,0]
	v_cvt_scalef32_pk_f32_fp4 v[140:141], v131, 1.0 op_sel:[0,1,0]
	v_cvt_scalef32_pk_f32_fp4 v[142:143], v131, 1.0 op_sel:[1,1,0]
	v_add_f32_e32 v5, v5, v7
	v_pk_fma_f32 v[8:9], v[60:61], v[136:137], v[8:9]
	v_pk_fma_f32 v[10:11], v[62:63], v[138:139], v[10:11]
	v_pk_fma_f32 v[12:13], v[64:65], v[140:141], v[12:13]
	v_pk_fma_f32 v[14:15], v[80:81], v[142:143], v[14:15]
	v_readlane_b32 s74, v5, 63
	v_cvt_scalef32_pk_f32_fp4 v[136:137], v132, 1.0
	v_cvt_scalef32_pk_f32_fp4 v[138:139], v132, 1.0 op_sel:[1,0,0]
	v_cvt_scalef32_pk_f32_fp4 v[140:141], v132, 1.0 op_sel:[0,1,0]
	v_cvt_scalef32_pk_f32_fp4 v[142:143], v132, 1.0 op_sel:[1,1,0]
	s_lshl_b64 exec, 1, s32
	v_mov_b32_e32 v125, s74
	s_mov_b64 exec, -1
	v_pk_fma_f32 v[8:9], v[82:83], v[136:137], v[8:9]
	v_pk_fma_f32 v[10:11], v[84:85], v[138:139], v[10:11]
	v_pk_fma_f32 v[12:13], v[86:87], v[140:141], v[12:13]
	v_pk_fma_f32 v[14:15], v[88:89], v[142:143], v[14:15]
	v_cvt_scalef32_pk_f32_fp4 v[136:137], v133, 1.0
	v_cvt_scalef32_pk_f32_fp4 v[138:139], v133, 1.0 op_sel:[1,0,0]
	v_cvt_scalef32_pk_f32_fp4 v[140:141], v133, 1.0 op_sel:[0,1,0]
	v_cvt_scalef32_pk_f32_fp4 v[142:143], v133, 1.0 op_sel:[1,1,0]
	v_pk_fma_f32 v[8:9], v[90:91], v[136:137], v[8:9]
	v_pk_fma_f32 v[10:11], v[92:93], v[138:139], v[10:11]
	v_pk_fma_f32 v[12:13], v[94:95], v[140:141], v[12:13]
	v_pk_fma_f32 v[14:15], v[96:97], v[142:143], v[14:15]
	v_pk_add_f32 v[8:9], v[8:9], v[10:11]
	v_pk_add_f32 v[12:13], v[12:13], v[14:15]
	v_pk_add_f32 v[8:9], v[8:9], v[12:13]
	v_add_f32_e32 v6, v8, v9
	s_mov_b32 s32, 63
	v_add_f32_dpp v6, v6, v6 quad_perm:[1,0,3,2] row_mask:0xf bank_mask:0xf bound_ctrl:1
	s_nop 1
	v_add_f32_dpp v6, v6, v6 quad_perm:[2,3,0,1] row_mask:0xf bank_mask:0xf bound_ctrl:1
	s_nop 1
	v_add_f32_dpp v6, v6, v6 row_half_mirror row_mask:0xf bank_mask:0xf bound_ctrl:1
	s_nop 1
	v_mov_b32_e32 v7, 0
	s_nop 1
	v_add_f32_dpp v6, v6, v6 row_mirror row_mask:0xf bank_mask:0xf bound_ctrl:1
	s_nop 1
	v_mov_b32_dpp v7, v6 row_bcast:15 row_mask:0xa bank_mask:0xf
	s_nop 1
	v_add_f32_e32 v6, v6, v7
	s_nop 1
	v_mov_b32_e32 v7, 0
	s_nop 1
	v_mov_b32_dpp v7, v6 row_bcast:31 row_mask:0xc bank_mask:0xf
	s_nop 1
	v_add_f32_e32 v6, v6, v7
	s_nop 1
	v_readlane_b32 s74, v6, 63
	s_nop 1
	s_lshl_b64 exec, 1, s32
	v_mov_b32_e32 v125, s74
	s_mov_b64 exec, -1
	s_nop 1
	s_nop 1
	v_mul_f32_e32 v16, v121, v120
	v_fma_f32 v17, |v16|, s96, 1.0
	v_rcp_f32_e32 v17, v17
	v_cmp_gt_f32_e32 vcc, 0, v16
	v_mul_f32_e32 v18, v16, v16
	v_mul_f32_e32 v18, 0xbf38aa3b, v18
	v_exp_f32_e32 v18, v18
	v_fmamk_f32 v120, v17, 0x3f07dc22, v117
	v_fmaak_f32 v120, v17, v120, 0x3f35f0e3
	v_fmaak_f32 v120, v17, v120, 0xbe11a98e
	v_fmaak_f32 v120, v17, v120, 0x3e027906
	v_mul_f32_e32 v17, v17, v120
	v_mul_f32_e32 v17, v18, v17
	v_mul_f32_e32 v18, v16, v17
	v_fma_f32 v16, -v16, v17, v16
	v_cndmask_b32_e32 v16, v16, v18, vcc
	v_mul_f32_e32 v120, v124, v16
	v_mul_f32_e32 v16, v119, v125
	v_fma_f32 v17, |v16|, s96, 1.0
	v_rcp_f32_e32 v17, v17
	v_cmp_gt_f32_e32 vcc, 0, v16
	v_mul_f32_e32 v18, v16, v16
	v_mul_f32_e32 v18, 0xbf38aa3b, v18
	v_exp_f32_e32 v18, v18
	v_fmamk_f32 v125, v17, 0x3f07dc22, v117
	v_fmaak_f32 v125, v17, v125, 0x3f35f0e3
	v_fmaak_f32 v125, v17, v125, 0xbe11a98e
	v_fmaak_f32 v125, v17, v125, 0x3e027906
	v_mul_f32_e32 v17, v17, v125
	v_mul_f32_e32 v17, v18, v17
	v_mul_f32_e32 v18, v16, v17
	v_fma_f32 v16, -v16, v17, v16
	v_cndmask_b32_e32 v16, v16, v18, vcc
	v_mul_f32_e32 v125, v122, v16
	v_mov_b32_e32 v94, 0
	s_movk_i32 s46, 0x80
	s_mov_b32 s47, 0
	v_mov_b32_e32 v95, v94
	v_mov_b32_e32 v96, v94
	v_mov_b32_e32 v97, v94
	v_mov_b32_e32 v92, v94
	v_mov_b32_e32 v93, v94
	v_mov_b32_e32 v90, v94
	v_mov_b32_e32 v91, v94
	v_mov_b32_e32 v88, v94
	v_mov_b32_e32 v89, v94
	v_mov_b32_e32 v86, v94
	v_mov_b32_e32 v87, v94
	v_mov_b32_e32 v84, v94
	v_mov_b32_e32 v85, v94
	v_mov_b32_e32 v82, v94
	v_mov_b32_e32 v83, v94
	v_mov_b32_e32 v64, v94
	v_mov_b32_e32 v65, v94
	v_mov_b32_e32 v80, v94
	v_mov_b32_e32 v81, v94
	v_mov_b32_e32 v62, v94
	v_mov_b32_e32 v63, v94
	v_mov_b32_e32 v60, v94
	v_mov_b32_e32 v61, v94
	v_mov_b32_e32 v58, v94
	v_mov_b32_e32 v59, v94
	v_mov_b32_e32 v56, v94
	v_mov_b32_e32 v57, v94
	v_mov_b32_e32 v54, v94
	v_mov_b32_e32 v55, v94
	v_mov_b32_e32 v52, v94
	v_mov_b32_e32 v53, v94
	v_mov_b32_e32 v50, v94
	v_mov_b32_e32 v51, v94
	v_mov_b32_e32 v48, v94
	v_mov_b32_e32 v49, v94
	v_mov_b32_e32 v46, v94
	v_mov_b32_e32 v47, v94
	v_mov_b32_e32 v44, v94
	v_mov_b32_e32 v45, v94
	v_mov_b32_e32 v42, v94
	v_mov_b32_e32 v43, v94
	v_mov_b32_e32 v40, v94
	v_mov_b32_e32 v41, v94
	v_mov_b32_e32 v38, v94
	v_mov_b32_e32 v39, v94
	v_mov_b32_e32 v36, v94
	v_mov_b32_e32 v37, v94
	v_mov_b32_e32 v32, v94
	v_mov_b32_e32 v33, v94
	v_mov_b32_e32 v34, v94
	v_mov_b32_e32 v35, v94
	v_mov_b32_e32 v30, v94
	v_mov_b32_e32 v31, v94
	v_mov_b32_e32 v28, v94
	v_mov_b32_e32 v29, v94
	v_mov_b32_e32 v26, v94
	v_mov_b32_e32 v27, v94
	v_mov_b32_e32 v24, v94
	v_mov_b32_e32 v25, v94
	v_mov_b32_e32 v20, v94
	v_mov_b32_e32 v21, v94
	v_mov_b32_e32 v22, v94
	v_mov_b32_e32 v23, v94
; DI void peer_token(LAS unsigned char* ring, const bf16* x1row, float inv2, const float* nffn, const int* ex, const float* pg, const unsigned char* U6, const unsigned char* V6,
;                    const float* usc, const float* vsc, float* orow, int lane) {
;     ...
;     for (int k = 0; k < 56; ++k) P11_V(k, cf_lo, vl, e_lo, k + 8);
; #pragma unroll 1
;     for (int k = 56; k < 64; ++k) P11_V(k, cf_lo, vl, e_hi, k - 56);
.Lv_sweep_lo:
	s_add_i32 s47, s46, 1
	s_and_b32 s47, s47, 7
	s_lshl_b32 s47, s47, 11
	s_add_i32 s77, s33, s47
	v_add_u32_e32 v4, s77, v70
	s_add_i32 s78, s46, 9
	s_and_b32 s75, s78, 0x7f
	v_readlane_b32 s79, v113, s75
	v_readlane_b32 s47, v112, s75
	s_bitcmp1_b32 s75, 6
	s_cselect_b32 s47, s79, s47
	s_lshl_b32 s47, s47, 11
	s_bitcmp1_b32 s78, 7
	s_cselect_b32 s78, s98, 0
	s_cselect_b32 s79, s99, 0
	s_add_u32 s78, s78, s47
	s_addc_u32 s79, s79, 0
	v_readlane_b32 s74, v120, s46
	s_waitcnt vmcnt(14)
	ds_read_b128 v[126:129], v4
	ds_read_b128 v[130:133], v4 offset:1024
	v_lshl_add_u64 v[2:3], v[72:73], 0, s[78:79]
	v_cvt_scalef32_pk_f32_fp4 v[136:137], v98, 1.0
	v_cvt_scalef32_pk_f32_fp4 v[138:139], v98, 1.0 op_sel:[1,0,0]
	v_cvt_scalef32_pk_f32_fp4 v[140:141], v98, 1.0 op_sel:[0,1,0]
	v_cvt_scalef32_pk_f32_fp4 v[142:143], v98, 1.0 op_sel:[1,1,0]
	v_pk_fma_f32 v[94:95], s[74:75], v[136:137], v[94:95] op_sel_hi:[0,1,1]
	v_pk_fma_f32 v[96:97], s[74:75], v[138:139], v[96:97] op_sel_hi:[0,1,1]
	v_pk_fma_f32 v[92:93], s[74:75], v[140:141], v[92:93] op_sel_hi:[0,1,1]
	v_pk_fma_f32 v[90:91], s[74:75], v[142:143], v[90:91] op_sel_hi:[0,1,1]
	v_cvt_scalef32_pk_f32_fp4 v[136:137], v99, 1.0
	v_cvt_scalef32_pk_f32_fp4 v[138:139], v99, 1.0 op_sel:[1,0,0]
	v_cvt_scalef32_pk_f32_fp4 v[140:141], v99, 1.0 op_sel:[0,1,0]
	v_cvt_scalef32_pk_f32_fp4 v[142:143], v99, 1.0 op_sel:[1,1,0]
	v_pk_fma_f32 v[88:89], s[74:75], v[136:137], v[88:89] op_sel_hi:[0,1,1]
	v_pk_fma_f32 v[86:87], s[74:75], v[138:139], v[86:87] op_sel_hi:[0,1,1]
	v_pk_fma_f32 v[84:85], s[74:75], v[140:141], v[84:85] op_sel_hi:[0,1,1]
	v_pk_fma_f32 v[82:83], s[74:75], v[142:143], v[82:83] op_sel_hi:[0,1,1]
	v_cvt_scalef32_pk_f32_fp4 v[136:137], v100, 1.0
	v_cvt_scalef32_pk_f32_fp4 v[138:139], v100, 1.0 op_sel:[1,0,0]
	v_cvt_scalef32_pk_f32_fp4 v[140:141], v100, 1.0 op_sel:[0,1,0]
	v_cvt_scalef32_pk_f32_fp4 v[142:143], v100, 1.0 op_sel:[1,1,0]
	v_pk_fma_f32 v[64:65], s[74:75], v[136:137], v[64:65] op_sel_hi:[0,1,1]
	v_pk_fma_f32 v[80:81], s[74:75], v[138:139], v[80:81] op_sel_hi:[0,1,1]
	v_pk_fma_f32 v[62:63], s[74:75], v[140:141], v[62:63] op_sel_hi:[0,1,1]
	v_pk_fma_f32 v[60:61], s[74:75], v[142:143], v[60:61] op_sel_hi:[0,1,1]
	s_waitcnt lgkmcnt(0)
	s_mov_b32 m0, s77
	s_nop 0
	global_load_lds_dwordx4 v[2:3], off
	global_load_lds_dwordx4 v[2:3], off offset:1024
	v_cvt_scalef32_pk_f32_fp4 v[136:137], v101, 1.0
	v_cvt_scalef32_pk_f32_fp4 v[138:139], v101, 1.0 op_sel:[1,0,0]
	v_cvt_scalef32_pk_f32_fp4 v[140:141], v101, 1.0 op_sel:[0,1,0]
	v_cvt_scalef32_pk_f32_fp4 v[142:143], v101, 1.0 op_sel:[1,1,0]
	v_pk_fma_f32 v[58:59], s[74:75], v[136:137], v[58:59] op_sel_hi:[0,1,1]
	v_pk_fma_f32 v[56:57], s[74:75], v[138:139], v[56:57] op_sel_hi:[0,1,1]
	v_pk_fma_f32 v[54:55], s[74:75], v[140:141], v[54:55] op_sel_hi:[0,1,1]
	v_pk_fma_f32 v[52:53], s[74:75], v[142:143], v[52:53] op_sel_hi:[0,1,1]
	v_cvt_scalef32_pk_f32_fp4 v[136:137], v102, 1.0
	v_cvt_scalef32_pk_f32_fp4 v[138:139], v102, 1.0 op_sel:[1,0,0]
	v_cvt_scalef32_pk_f32_fp4 v[140:141], v102, 1.0 op_sel:[0,1,0]
	v_cvt_scalef32_pk_f32_fp4 v[142:143], v102, 1.0 op_sel:[1,1,0]
	v_pk_fma_f32 v[50:51], s[74:75], v[136:137], v[50:51] op_sel_hi:[0,1,1]
	v_pk_fma_f32 v[48:49], s[74:75], v[138:139], v[48:49] op_sel_hi:[0,1,1]
	v_pk_fma_f32 v[46:47], s[74:75], v[140:141], v[46:47] op_sel_hi:[0,1,1]
	v_pk_fma_f32 v[44:45], s[74:75], v[142:143], v[44:45] op_sel_hi:[0,1,1]
	v_cvt_scalef32_pk_f32_fp4 v[136:137], v103, 1.0
	v_cvt_scalef32_pk_f32_fp4 v[138:139], v103, 1.0 op_sel:[1,0,0]
	v_cvt_scalef32_pk_f32_fp4 v[140:141], v103, 1.0 op_sel:[0,1,0]
	v_cvt_scalef32_pk_f32_fp4 v[142:143], v103, 1.0 op_sel:[1,1,0]
	v_pk_fma_f32 v[42:43], s[74:75], v[136:137], v[42:43] op_sel_hi:[0,1,1]
	v_pk_fma_f32 v[40:41], s[74:75], v[138:139], v[40:41] op_sel_hi:[0,1,1]
	v_pk_fma_f32 v[38:39], s[74:75], v[140:141], v[38:39] op_sel_hi:[0,1,1]
	v_pk_fma_f32 v[36:37], s[74:75], v[142:143], v[36:37] op_sel_hi:[0,1,1]
	v_cvt_scalef32_pk_f32_fp4 v[136:137], v104, 1.0
	v_cvt_scalef32_pk_f32_fp4 v[138:139], v104, 1.0 op_sel:[1,0,0]
	v_cvt_scalef32_pk_f32_fp4 v[140:141], v104, 1.0 op_sel:[0,1,0]
	v_cvt_scalef32_pk_f32_fp4 v[142:143], v104, 1.0 op_sel:[1,1,0]
	v_pk_fma_f32 v[32:33], s[74:75], v[136:137], v[32:33] op_sel_hi:[0,1,1]
	v_pk_fma_f32 v[34:35], s[74:75], v[138:139], v[34:35] op_sel_hi:[0,1,1]
	v_pk_fma_f32 v[30:31], s[74:75], v[140:141], v[30:31] op_sel_hi:[0,1,1]
	v_pk_fma_f32 v[28:29], s[74:75], v[142:143], v[28:29] op_sel_hi:[0,1,1]
	v_cvt_scalef32_pk_f32_fp4 v[136:137], v105, 1.0
	v_cvt_scalef32_pk_f32_fp4 v[138:139], v105, 1.0 op_sel:[1,0,0]
	v_cvt_scalef32_pk_f32_fp4 v[140:141], v105, 1.0 op_sel:[0,1,0]
	v_cvt_scalef32_pk_f32_fp4 v[142:143], v105, 1.0 op_sel:[1,1,0]
	v_pk_fma_f32 v[26:27], s[74:75], v[136:137], v[26:27] op_sel_hi:[0,1,1]
	v_pk_fma_f32 v[24:25], s[74:75], v[138:139], v[24:25] op_sel_hi:[0,1,1]
	v_pk_fma_f32 v[20:21], s[74:75], v[140:141], v[20:21] op_sel_hi:[0,1,1]
	v_pk_fma_f32 v[22:23], s[74:75], v[142:143], v[22:23] op_sel_hi:[0,1,1]
	s_add_i32 s47, s46, 2
	s_and_b32 s47, s47, 7
	s_lshl_b32 s47, s47, 11
	s_add_i32 s77, s33, s47
	v_add_u32_e32 v4, s77, v70
	s_add_i32 s78, s46, 10
	s_and_b32 s75, s78, 0x7f
	v_readlane_b32 s79, v113, s75
	v_readlane_b32 s47, v112, s75
	s_bitcmp1_b32 s75, 6
	s_cselect_b32 s47, s79, s47
	s_lshl_b32 s47, s47, 11
	s_bitcmp1_b32 s78, 7
	s_cselect_b32 s78, s98, 0
	s_cselect_b32 s79, s99, 0
	s_add_u32 s78, s78, s47
	s_addc_u32 s79, s79, 0
	s_add_i32 s32, s46, 1
	v_readlane_b32 s74, v120, s32
	s_waitcnt vmcnt(14)
; DI void peer_token(LAS unsigned char* ring, const bf16* x1row, float inv2, const float* nffn, const int* ex, const float* pg, const unsigned char* U6, const unsigned char* V6,
;                    const float* usc, const float* vsc, float* orow, int lane) {
;     ...
;     for (int k = 0; k < 56; ++k) P11_V(k, cf_lo, vl, e_lo, k + 8);
; #pragma unroll 1
;     for (int k = 56; k < 64; ++k) P11_V(k, cf_lo, vl, e_hi, k - 56);
	ds_read_b128 v[98:101], v4
	ds_read_b128 v[102:105], v4 offset:1024
	v_lshl_add_u64 v[2:3], v[72:73], 0, s[78:79]
	v_cvt_scalef32_pk_f32_fp4 v[136:137], v126, 1.0
	v_cvt_scalef32_pk_f32_fp4 v[138:139], v126, 1.0 op_sel:[1,0,0]
	v_cvt_scalef32_pk_f32_fp4 v[140:141], v126, 1.0 op_sel:[0,1,0]
	v_cvt_scalef32_pk_f32_fp4 v[142:143], v126, 1.0 op_sel:[1,1,0]
	v_pk_fma_f32 v[94:95], s[74:75], v[136:137], v[94:95] op_sel_hi:[0,1,1]
	v_pk_fma_f32 v[96:97], s[74:75], v[138:139], v[96:97] op_sel_hi:[0,1,1]
	v_pk_fma_f32 v[92:93], s[74:75], v[140:141], v[92:93] op_sel_hi:[0,1,1]
	v_pk_fma_f32 v[90:91], s[74:75], v[142:143], v[90:91] op_sel_hi:[0,1,1]
	v_cvt_scalef32_pk_f32_fp4 v[136:137], v127, 1.0
	v_cvt_scalef32_pk_f32_fp4 v[138:139], v127, 1.0 op_sel:[1,0,0]
	v_cvt_scalef32_pk_f32_fp4 v[140:141], v127, 1.0 op_sel:[0,1,0]
	v_cvt_scalef32_pk_f32_fp4 v[142:143], v127, 1.0 op_sel:[1,1,0]
	v_pk_fma_f32 v[88:89], s[74:75], v[136:137], v[88:89] op_sel_hi:[0,1,1]
	v_pk_fma_f32 v[86:87], s[74:75], v[138:139], v[86:87] op_sel_hi:[0,1,1]
	v_pk_fma_f32 v[84:85], s[74:75], v[140:141], v[84:85] op_sel_hi:[0,1,1]
	v_pk_fma_f32 v[82:83], s[74:75], v[142:143], v[82:83] op_sel_hi:[0,1,1]
	v_cvt_scalef32_pk_f32_fp4 v[136:137], v128, 1.0
	v_cvt_scalef32_pk_f32_fp4 v[138:139], v128, 1.0 op_sel:[1,0,0]
	v_cvt_scalef32_pk_f32_fp4 v[140:141], v128, 1.0 op_sel:[0,1,0]
	v_cvt_scalef32_pk_f32_fp4 v[142:143], v128, 1.0 op_sel:[1,1,0]
	v_pk_fma_f32 v[64:65], s[74:75], v[136:137], v[64:65] op_sel_hi:[0,1,1]
	v_pk_fma_f32 v[80:81], s[74:75], v[138:139], v[80:81] op_sel_hi:[0,1,1]
	v_pk_fma_f32 v[62:63], s[74:75], v[140:141], v[62:63] op_sel_hi:[0,1,1]
	v_pk_fma_f32 v[60:61], s[74:75], v[142:143], v[60:61] op_sel_hi:[0,1,1]
	s_waitcnt lgkmcnt(0)
	s_mov_b32 m0, s77
	s_nop 0
	global_load_lds_dwordx4 v[2:3], off
	global_load_lds_dwordx4 v[2:3], off offset:1024
	v_cvt_scalef32_pk_f32_fp4 v[136:137], v129, 1.0
	v_cvt_scalef32_pk_f32_fp4 v[138:139], v129, 1.0 op_sel:[1,0,0]
	v_cvt_scalef32_pk_f32_fp4 v[140:141], v129, 1.0 op_sel:[0,1,0]
	v_cvt_scalef32_pk_f32_fp4 v[142:143], v129, 1.0 op_sel:[1,1,0]
	v_pk_fma_f32 v[58:59], s[74:75], v[136:137], v[58:59] op_sel_hi:[0,1,1]
	v_pk_fma_f32 v[56:57], s[74:75], v[138:139], v[56:57] op_sel_hi:[0,1,1]
	v_pk_fma_f32 v[54:55], s[74:75], v[140:141], v[54:55] op_sel_hi:[0,1,1]
	v_pk_fma_f32 v[52:53], s[74:75], v[142:143], v[52:53] op_sel_hi:[0,1,1]
	v_cvt_scalef32_pk_f32_fp4 v[136:137], v130, 1.0
	v_cvt_scalef32_pk_f32_fp4 v[138:139], v130, 1.0 op_sel:[1,0,0]
	v_cvt_scalef32_pk_f32_fp4 v[140:141], v130, 1.0 op_sel:[0,1,0]
	v_cvt_scalef32_pk_f32_fp4 v[142:143], v130, 1.0 op_sel:[1,1,0]
	v_pk_fma_f32 v[50:51], s[74:75], v[136:137], v[50:51] op_sel_hi:[0,1,1]
	v_pk_fma_f32 v[48:49], s[74:75], v[138:139], v[48:49] op_sel_hi:[0,1,1]
	v_pk_fma_f32 v[46:47], s[74:75], v[140:141], v[46:47] op_sel_hi:[0,1,1]
	v_pk_fma_f32 v[44:45], s[74:75], v[142:143], v[44:45] op_sel_hi:[0,1,1]
	v_cvt_scalef32_pk_f32_fp4 v[136:137], v131, 1.0
	v_cvt_scalef32_pk_f32_fp4 v[138:139], v131, 1.0 op_sel:[1,0,0]
	v_cvt_scalef32_pk_f32_fp4 v[140:141], v131, 1.0 op_sel:[0,1,0]
	v_cvt_scalef32_pk_f32_fp4 v[142:143], v131, 1.0 op_sel:[1,1,0]
	v_pk_fma_f32 v[42:43], s[74:75], v[136:137], v[42:43] op_sel_hi:[0,1,1]
	v_pk_fma_f32 v[40:41], s[74:75], v[138:139], v[40:41] op_sel_hi:[0,1,1]
	v_pk_fma_f32 v[38:39], s[74:75], v[140:141], v[38:39] op_sel_hi:[0,1,1]
	v_pk_fma_f32 v[36:37], s[74:75], v[142:143], v[36:37] op_sel_hi:[0,1,1]
	v_cvt_scalef32_pk_f32_fp4 v[136:137], v132, 1.0
	v_cvt_scalef32_pk_f32_fp4 v[138:139], v132, 1.0 op_sel:[1,0,0]
	v_cvt_scalef32_pk_f32_fp4 v[140:141], v132, 1.0 op_sel:[0,1,0]
	v_cvt_scalef32_pk_f32_fp4 v[142:143], v132, 1.0 op_sel:[1,1,0]
	v_pk_fma_f32 v[32:33], s[74:75], v[136:137], v[32:33] op_sel_hi:[0,1,1]
	v_pk_fma_f32 v[34:35], s[74:75], v[138:139], v[34:35] op_sel_hi:[0,1,1]
	v_pk_fma_f32 v[30:31], s[74:75], v[140:141], v[30:31] op_sel_hi:[0,1,1]
	v_pk_fma_f32 v[28:29], s[74:75], v[142:143], v[28:29] op_sel_hi:[0,1,1]
	v_cvt_scalef32_pk_f32_fp4 v[136:137], v133, 1.0
	v_cvt_scalef32_pk_f32_fp4 v[138:139], v133, 1.0 op_sel:[1,0,0]
	v_cvt_scalef32_pk_f32_fp4 v[140:141], v133, 1.0 op_sel:[0,1,0]
	v_cvt_scalef32_pk_f32_fp4 v[142:143], v133, 1.0 op_sel:[1,1,0]
	v_pk_fma_f32 v[26:27], s[74:75], v[136:137], v[26:27] op_sel_hi:[0,1,1]
	v_pk_fma_f32 v[24:25], s[74:75], v[138:139], v[24:25] op_sel_hi:[0,1,1]
	v_pk_fma_f32 v[20:21], s[74:75], v[140:141], v[20:21] op_sel_hi:[0,1,1]
	v_pk_fma_f32 v[22:23], s[74:75], v[142:143], v[22:23] op_sel_hi:[0,1,1]
	s_add_i32 s46, s46, 2
	s_cmp_lg_u32 s46, 192
	s_cbranch_scc1 .Lv_sweep_lo
; DI void peer_token(LAS unsigned char* ring, const bf16* x1row, float inv2, const float* nffn, const int* ex, const float* pg, const unsigned char* U6, const unsigned char* V6,
;                    const float* usc, const float* vsc, float* orow, int lane) {
;     ...
;     for (int k = 64; k < 120; ++k) P11_V(k, cf_hi, vl, e_hi, k - 56);
; #pragma unroll 1
;     for (int k = 120; k < 128; ++k) P11_V(k, cf_hi, vl, e_lo, k - 120);
.Lv_sweep_hi:
	s_add_i32 s47, s46, 1
	s_and_b32 s47, s47, 7
	s_lshl_b32 s47, s47, 11
	s_add_i32 s77, s33, s47
	v_add_u32_e32 v4, s77, v70
	s_add_i32 s78, s46, 9
	s_and_b32 s75, s78, 0x7f
	v_readlane_b32 s79, v113, s75
	v_readlane_b32 s47, v112, s75
	s_bitcmp1_b32 s75, 6
	s_cselect_b32 s47, s79, s47
	s_lshl_b32 s47, s47, 11
	s_bitcmp1_b32 s78, 7
	s_cselect_b32 s78, s98, 0
	s_cselect_b32 s79, s99, 0
	s_add_u32 s78, s78, s47
	s_addc_u32 s79, s79, 0
	v_readlane_b32 s74, v125, s46
	s_waitcnt vmcnt(14)
	ds_read_b128 v[126:129], v4
	ds_read_b128 v[130:133], v4 offset:1024
	v_lshl_add_u64 v[2:3], v[72:73], 0, s[78:79]
	v_cvt_scalef32_pk_f32_fp4 v[136:137], v98, 1.0
	v_cvt_scalef32_pk_f32_fp4 v[138:139], v98, 1.0 op_sel:[1,0,0]
	v_cvt_scalef32_pk_f32_fp4 v[140:141], v98, 1.0 op_sel:[0,1,0]
	v_cvt_scalef32_pk_f32_fp4 v[142:143], v98, 1.0 op_sel:[1,1,0]
	v_pk_fma_f32 v[94:95], s[74:75], v[136:137], v[94:95] op_sel_hi:[0,1,1]
	v_pk_fma_f32 v[96:97], s[74:75], v[138:139], v[96:97] op_sel_hi:[0,1,1]
	v_pk_fma_f32 v[92:93], s[74:75], v[140:141], v[92:93] op_sel_hi:[0,1,1]
	v_pk_fma_f32 v[90:91], s[74:75], v[142:143], v[90:91] op_sel_hi:[0,1,1]
	v_cvt_scalef32_pk_f32_fp4 v[136:137], v99, 1.0
	v_cvt_scalef32_pk_f32_fp4 v[138:139], v99, 1.0 op_sel:[1,0,0]
	v_cvt_scalef32_pk_f32_fp4 v[140:141], v99, 1.0 op_sel:[0,1,0]
	v_cvt_scalef32_pk_f32_fp4 v[142:143], v99, 1.0 op_sel:[1,1,0]
	v_pk_fma_f32 v[88:89], s[74:75], v[136:137], v[88:89] op_sel_hi:[0,1,1]
	v_pk_fma_f32 v[86:87], s[74:75], v[138:139], v[86:87] op_sel_hi:[0,1,1]
	v_pk_fma_f32 v[84:85], s[74:75], v[140:141], v[84:85] op_sel_hi:[0,1,1]
	v_pk_fma_f32 v[82:83], s[74:75], v[142:143], v[82:83] op_sel_hi:[0,1,1]
	v_cvt_scalef32_pk_f32_fp4 v[136:137], v100, 1.0
	v_cvt_scalef32_pk_f32_fp4 v[138:139], v100, 1.0 op_sel:[1,0,0]
	v_cvt_scalef32_pk_f32_fp4 v[140:141], v100, 1.0 op_sel:[0,1,0]
	v_cvt_scalef32_pk_f32_fp4 v[142:143], v100, 1.0 op_sel:[1,1,0]
	v_pk_fma_f32 v[64:65], s[74:75], v[136:137], v[64:65] op_sel_hi:[0,1,1]
	v_pk_fma_f32 v[80:81], s[74:75], v[138:139], v[80:81] op_sel_hi:[0,1,1]
	v_pk_fma_f32 v[62:63], s[74:75], v[140:141], v[62:63] op_sel_hi:[0,1,1]
	v_pk_fma_f32 v[60:61], s[74:75], v[142:143], v[60:61] op_sel_hi:[0,1,1]
	s_waitcnt lgkmcnt(0)
	s_mov_b32 m0, s77
	s_nop 0
	global_load_lds_dwordx4 v[2:3], off
	global_load_lds_dwordx4 v[2:3], off offset:1024
	v_cvt_scalef32_pk_f32_fp4 v[136:137], v101, 1.0
	v_cvt_scalef32_pk_f32_fp4 v[138:139], v101, 1.0 op_sel:[1,0,0]
	v_cvt_scalef32_pk_f32_fp4 v[140:141], v101, 1.0 op_sel:[0,1,0]
	v_cvt_scalef32_pk_f32_fp4 v[142:143], v101, 1.0 op_sel:[1,1,0]
	v_pk_fma_f32 v[58:59], s[74:75], v[136:137], v[58:59] op_sel_hi:[0,1,1]
	v_pk_fma_f32 v[56:57], s[74:75], v[138:139], v[56:57] op_sel_hi:[0,1,1]
	v_pk_fma_f32 v[54:55], s[74:75], v[140:141], v[54:55] op_sel_hi:[0,1,1]
	v_pk_fma_f32 v[52:53], s[74:75], v[142:143], v[52:53] op_sel_hi:[0,1,1]
	v_cvt_scalef32_pk_f32_fp4 v[136:137], v102, 1.0
	v_cvt_scalef32_pk_f32_fp4 v[138:139], v102, 1.0 op_sel:[1,0,0]
	v_cvt_scalef32_pk_f32_fp4 v[140:141], v102, 1.0 op_sel:[0,1,0]
	v_cvt_scalef32_pk_f32_fp4 v[142:143], v102, 1.0 op_sel:[1,1,0]
	v_pk_fma_f32 v[50:51], s[74:75], v[136:137], v[50:51] op_sel_hi:[0,1,1]
	v_pk_fma_f32 v[48:49], s[74:75], v[138:139], v[48:49] op_sel_hi:[0,1,1]
	v_pk_fma_f32 v[46:47], s[74:75], v[140:141], v[46:47] op_sel_hi:[0,1,1]
	v_pk_fma_f32 v[44:45], s[74:75], v[142:143], v[44:45] op_sel_hi:[0,1,1]
	v_cvt_scalef32_pk_f32_fp4 v[136:137], v103, 1.0
	v_cvt_scalef32_pk_f32_fp4 v[138:139], v103, 1.0 op_sel:[1,0,0]
	v_cvt_scalef32_pk_f32_fp4 v[140:141], v103, 1.0 op_sel:[0,1,0]
	v_cvt_scalef32_pk_f32_fp4 v[142:143], v103, 1.0 op_sel:[1,1,0]
	v_pk_fma_f32 v[42:43], s[74:75], v[136:137], v[42:43] op_sel_hi:[0,1,1]
	v_pk_fma_f32 v[40:41], s[74:75], v[138:139], v[40:41] op_sel_hi:[0,1,1]
	v_pk_fma_f32 v[38:39], s[74:75], v[140:141], v[38:39] op_sel_hi:[0,1,1]
	v_pk_fma_f32 v[36:37], s[74:75], v[142:143], v[36:37] op_sel_hi:[0,1,1]
	v_cvt_scalef32_pk_f32_fp4 v[136:137], v104, 1.0
	v_cvt_scalef32_pk_f32_fp4 v[138:139], v104, 1.0 op_sel:[1,0,0]
	v_cvt_scalef32_pk_f32_fp4 v[140:141], v104, 1.0 op_sel:[0,1,0]
	v_cvt_scalef32_pk_f32_fp4 v[142:143], v104, 1.0 op_sel:[1,1,0]
	v_pk_fma_f32 v[32:33], s[74:75], v[136:137], v[32:33] op_sel_hi:[0,1,1]
	v_pk_fma_f32 v[34:35], s[74:75], v[138:139], v[34:35] op_sel_hi:[0,1,1]
	v_pk_fma_f32 v[30:31], s[74:75], v[140:141], v[30:31] op_sel_hi:[0,1,1]
	v_pk_fma_f32 v[28:29], s[74:75], v[142:143], v[28:29] op_sel_hi:[0,1,1]
	v_cvt_scalef32_pk_f32_fp4 v[136:137], v105, 1.0
	v_cvt_scalef32_pk_f32_fp4 v[138:139], v105, 1.0 op_sel:[1,0,0]
	v_cvt_scalef32_pk_f32_fp4 v[140:141], v105, 1.0 op_sel:[0,1,0]
	v_cvt_scalef32_pk_f32_fp4 v[142:143], v105, 1.0 op_sel:[1,1,0]
	v_pk_fma_f32 v[26:27], s[74:75], v[136:137], v[26:27] op_sel_hi:[0,1,1]
	v_pk_fma_f32 v[24:25], s[74:75], v[138:139], v[24:25] op_sel_hi:[0,1,1]
	v_pk_fma_f32 v[20:21], s[74:75], v[140:141], v[20:21] op_sel_hi:[0,1,1]
	v_pk_fma_f32 v[22:23], s[74:75], v[142:143], v[22:23] op_sel_hi:[0,1,1]
	s_add_i32 s47, s46, 2
	s_and_b32 s47, s47, 7
	s_lshl_b32 s47, s47, 11
	s_add_i32 s77, s33, s47
	v_add_u32_e32 v4, s77, v70
	s_add_i32 s78, s46, 10
	s_and_b32 s75, s78, 0x7f
	v_readlane_b32 s79, v113, s75
	v_readlane_b32 s47, v112, s75
	s_bitcmp1_b32 s75, 6
	s_cselect_b32 s47, s79, s47
	s_lshl_b32 s47, s47, 11
	s_bitcmp1_b32 s78, 7
	s_cselect_b32 s78, s98, 0
	s_cselect_b32 s79, s99, 0
	s_add_u32 s78, s78, s47
	s_addc_u32 s79, s79, 0
	s_add_i32 s32, s46, 1
	v_readlane_b32 s74, v125, s32
	s_waitcnt vmcnt(14)
; DI void peer_token(LAS unsigned char* ring, const bf16* x1row, float inv2, const float* nffn, const int* ex, const float* pg, const unsigned char* U6, const unsigned char* V6,
;                    const float* usc, const float* vsc, float* orow, int lane) {
;     ...
;     for (int k = 64; k < 120; ++k) P11_V(k, cf_hi, vl, e_hi, k - 56);
; #pragma unroll 1
;     for (int k = 120; k < 128; ++k) P11_V(k, cf_hi, vl, e_lo, k - 120);
	ds_read_b128 v[98:101], v4
	ds_read_b128 v[102:105], v4 offset:1024
	v_lshl_add_u64 v[2:3], v[72:73], 0, s[78:79]
	v_cvt_scalef32_pk_f32_fp4 v[136:137], v126, 1.0
	v_cvt_scalef32_pk_f32_fp4 v[138:139], v126, 1.0 op_sel:[1,0,0]
	v_cvt_scalef32_pk_f32_fp4 v[140:141], v126, 1.0 op_sel:[0,1,0]
	v_cvt_scalef32_pk_f32_fp4 v[142:143], v126, 1.0 op_sel:[1,1,0]
	v_pk_fma_f32 v[94:95], s[74:75], v[136:137], v[94:95] op_sel_hi:[0,1,1]
	v_pk_fma_f32 v[96:97], s[74:75], v[138:139], v[96:97] op_sel_hi:[0,1,1]
	v_pk_fma_f32 v[92:93], s[74:75], v[140:141], v[92:93] op_sel_hi:[0,1,1]
	v_pk_fma_f32 v[90:91], s[74:75], v[142:143], v[90:91] op_sel_hi:[0,1,1]
	v_cvt_scalef32_pk_f32_fp4 v[136:137], v127, 1.0
	v_cvt_scalef32_pk_f32_fp4 v[138:139], v127, 1.0 op_sel:[1,0,0]
	v_cvt_scalef32_pk_f32_fp4 v[140:141], v127, 1.0 op_sel:[0,1,0]
	v_cvt_scalef32_pk_f32_fp4 v[142:143], v127, 1.0 op_sel:[1,1,0]
	v_pk_fma_f32 v[88:89], s[74:75], v[136:137], v[88:89] op_sel_hi:[0,1,1]
	v_pk_fma_f32 v[86:87], s[74:75], v[138:139], v[86:87] op_sel_hi:[0,1,1]
	v_pk_fma_f32 v[84:85], s[74:75], v[140:141], v[84:85] op_sel_hi:[0,1,1]
	v_pk_fma_f32 v[82:83], s[74:75], v[142:143], v[82:83] op_sel_hi:[0,1,1]
	v_cvt_scalef32_pk_f32_fp4 v[136:137], v128, 1.0
	v_cvt_scalef32_pk_f32_fp4 v[138:139], v128, 1.0 op_sel:[1,0,0]
	v_cvt_scalef32_pk_f32_fp4 v[140:141], v128, 1.0 op_sel:[0,1,0]
	v_cvt_scalef32_pk_f32_fp4 v[142:143], v128, 1.0 op_sel:[1,1,0]
	v_pk_fma_f32 v[64:65], s[74:75], v[136:137], v[64:65] op_sel_hi:[0,1,1]
	v_pk_fma_f32 v[80:81], s[74:75], v[138:139], v[80:81] op_sel_hi:[0,1,1]
	v_pk_fma_f32 v[62:63], s[74:75], v[140:141], v[62:63] op_sel_hi:[0,1,1]
	v_pk_fma_f32 v[60:61], s[74:75], v[142:143], v[60:61] op_sel_hi:[0,1,1]
	s_waitcnt lgkmcnt(0)
	s_mov_b32 m0, s77
	s_nop 0
	global_load_lds_dwordx4 v[2:3], off
	global_load_lds_dwordx4 v[2:3], off offset:1024
	v_cvt_scalef32_pk_f32_fp4 v[136:137], v129, 1.0
	v_cvt_scalef32_pk_f32_fp4 v[138:139], v129, 1.0 op_sel:[1,0,0]
	v_cvt_scalef32_pk_f32_fp4 v[140:141], v129, 1.0 op_sel:[0,1,0]
	v_cvt_scalef32_pk_f32_fp4 v[142:143], v129, 1.0 op_sel:[1,1,0]
	v_pk_fma_f32 v[58:59], s[74:75], v[136:137], v[58:59] op_sel_hi:[0,1,1]
	v_pk_fma_f32 v[56:57], s[74:75], v[138:139], v[56:57] op_sel_hi:[0,1,1]
	v_pk_fma_f32 v[54:55], s[74:75], v[140:141], v[54:55] op_sel_hi:[0,1,1]
	v_pk_fma_f32 v[52:53], s[74:75], v[142:143], v[52:53] op_sel_hi:[0,1,1]
	v_cvt_scalef32_pk_f32_fp4 v[136:137], v130, 1.0
	v_cvt_scalef32_pk_f32_fp4 v[138:139], v130, 1.0 op_sel:[1,0,0]
	v_cvt_scalef32_pk_f32_fp4 v[140:141], v130, 1.0 op_sel:[0,1,0]
	v_cvt_scalef32_pk_f32_fp4 v[142:143], v130, 1.0 op_sel:[1,1,0]
	v_pk_fma_f32 v[50:51], s[74:75], v[136:137], v[50:51] op_sel_hi:[0,1,1]
	v_pk_fma_f32 v[48:49], s[74:75], v[138:139], v[48:49] op_sel_hi:[0,1,1]
	v_pk_fma_f32 v[46:47], s[74:75], v[140:141], v[46:47] op_sel_hi:[0,1,1]
	v_pk_fma_f32 v[44:45], s[74:75], v[142:143], v[44:45] op_sel_hi:[0,1,1]
	v_cvt_scalef32_pk_f32_fp4 v[136:137], v131, 1.0
	v_cvt_scalef32_pk_f32_fp4 v[138:139], v131, 1.0 op_sel:[1,0,0]
	v_cvt_scalef32_pk_f32_fp4 v[140:141], v131, 1.0 op_sel:[0,1,0]
	v_cvt_scalef32_pk_f32_fp4 v[142:143], v131, 1.0 op_sel:[1,1,0]
	v_pk_fma_f32 v[42:43], s[74:75], v[136:137], v[42:43] op_sel_hi:[0,1,1]
	v_pk_fma_f32 v[40:41], s[74:75], v[138:139], v[40:41] op_sel_hi:[0,1,1]
	v_pk_fma_f32 v[38:39], s[74:75], v[140:141], v[38:39] op_sel_hi:[0,1,1]
	v_pk_fma_f32 v[36:37], s[74:75], v[142:143], v[36:37] op_sel_hi:[0,1,1]
	v_cvt_scalef32_pk_f32_fp4 v[136:137], v132, 1.0
	v_cvt_scalef32_pk_f32_fp4 v[138:139], v132, 1.0 op_sel:[1,0,0]
	v_cvt_scalef32_pk_f32_fp4 v[140:141], v132, 1.0 op_sel:[0,1,0]
	v_cvt_scalef32_pk_f32_fp4 v[142:143], v132, 1.0 op_sel:[1,1,0]
	v_pk_fma_f32 v[32:33], s[74:75], v[136:137], v[32:33] op_sel_hi:[0,1,1]
	v_pk_fma_f32 v[34:35], s[74:75], v[138:139], v[34:35] op_sel_hi:[0,1,1]
	v_pk_fma_f32 v[30:31], s[74:75], v[140:141], v[30:31] op_sel_hi:[0,1,1]
	v_pk_fma_f32 v[28:29], s[74:75], v[142:143], v[28:29] op_sel_hi:[0,1,1]
	v_cvt_scalef32_pk_f32_fp4 v[136:137], v133, 1.0
	v_cvt_scalef32_pk_f32_fp4 v[138:139], v133, 1.0 op_sel:[1,0,0]
	v_cvt_scalef32_pk_f32_fp4 v[140:141], v133, 1.0 op_sel:[0,1,0]
	v_cvt_scalef32_pk_f32_fp4 v[142:143], v133, 1.0 op_sel:[1,1,0]
	v_pk_fma_f32 v[26:27], s[74:75], v[136:137], v[26:27] op_sel_hi:[0,1,1]
	v_pk_fma_f32 v[24:25], s[74:75], v[138:139], v[24:25] op_sel_hi:[0,1,1]
	v_pk_fma_f32 v[20:21], s[74:75], v[140:141], v[20:21] op_sel_hi:[0,1,1]
	v_pk_fma_f32 v[22:23], s[74:75], v[142:143], v[22:23] op_sel_hi:[0,1,1]
	s_add_i32 s46, s46, 2
	s_cmp_lg_u32 s46, 256
	s_cbranch_scc1 .Lv_sweep_hi
; DI void peer_token(LAS unsigned char* ring, const bf16* x1row, float inv2, const float* nffn, const int* ex, const float* pg, const unsigned char* U6, const unsigned char* V6,
;                    const float* usc, const float* vsc, float* orow, int lane) {
;     ...
;     const float ysc = 1.0f;
;     asm volatile("s_waitcnt vmcnt(0)" ::: "memory");
; #pragma unroll
;     for (int i = 0; i < 16; ++i) {
;         const v2u aw = *(const v2u*)(x1row + i * 256 + lane * 4);
;         *(f32x4*)(orow + i * 256 + lane * 4) = (f32x4){bflo(aw.x) + ysc * y[2 * i].x, bfhi(aw.x) + ysc * y[2 * i].y, bflo(aw.y) + ysc * y[2 * i + 1].x, bfhi(aw.y) + ysc * y[2 * i + 1].y};
;     }
; __global__ void __launch_bounds__(NTHREADS, 2) fwd(Args args) {
;     ...
; #pragma unroll 1
;             for (int j = 0; j < 4; ++j) { const int t = tb * 32 + wave * 4 + j;
;                 peer_token(lds + wave * (4 * RSLOT), XB + (size_t)t * DM, inv2[t], norm_ffn, experts + (size_t)t * 128, pgates + (size_t)t * 128, U8, V8, usc, vsc, out + (size_t)t * DM, lane); }
;             __syncthreads();
;         }
	s_waitcnt vmcnt(0)
	v_lshl_add_u64 v[98:99], s[44:45], 2, v[76:77]
	s_add_i32 s76, s76, 1
	s_cmp_eq_u32 s76, 4
	v_add_co_u32_e32 v100, vcc, s81, v98
	s_nop 1
	v_addc_co_u32_e32 v101, vcc, 0, v99, vcc
	v_add_co_u32_e32 v102, vcc, s84, v98
	s_nop 1
	v_addc_co_u32_e32 v103, vcc, 0, v99, vcc
	v_lshlrev_b32_e32 v2, 16, v146
	v_and_b32_e32 v3, 0xffff0000, v146
	v_lshlrev_b32_e32 v4, 16, v147
	v_and_b32_e32 v5, 0xffff0000, v147
	v_pk_add_f32 v[2:3], v[94:95], v[2:3]
	v_pk_add_f32 v[4:5], v[96:97], v[4:5]
	global_store_dwordx4 v[98:99], v[2:5], off
	v_lshlrev_b32_e32 v10, 16, v148
	v_and_b32_e32 v11, 0xffff0000, v148
	v_lshlrev_b32_e32 v12, 16, v149
	v_and_b32_e32 v13, 0xffff0000, v149
	v_pk_add_f32 v[10:11], v[92:93], v[10:11]
	v_pk_add_f32 v[12:13], v[90:91], v[12:13]
	global_store_dwordx4 v[98:99], v[10:13], off offset:1024
	v_lshlrev_b32_e32 v14, 16, v150
	v_and_b32_e32 v15, 0xffff0000, v150
	v_lshlrev_b32_e32 v16, 16, v151
	v_and_b32_e32 v17, 0xffff0000, v151
	v_pk_add_f32 v[14:15], v[88:89], v[14:15]
	v_pk_add_f32 v[16:17], v[86:87], v[16:17]
	global_store_dwordx4 v[98:99], v[14:17], off offset:2048
	v_lshlrev_b32_e32 v2, 16, v152
	v_and_b32_e32 v3, 0xffff0000, v152
	v_lshlrev_b32_e32 v4, 16, v153
	v_and_b32_e32 v5, 0xffff0000, v153
	v_pk_add_f32 v[2:3], v[84:85], v[2:3]
	v_pk_add_f32 v[4:5], v[82:83], v[4:5]
	global_store_dwordx4 v[98:99], v[2:5], off offset:3072
	v_lshlrev_b32_e32 v10, 16, v154
	v_and_b32_e32 v11, 0xffff0000, v154
	v_lshlrev_b32_e32 v12, 16, v155
	v_and_b32_e32 v13, 0xffff0000, v155
	v_pk_add_f32 v[10:11], v[64:65], v[10:11]
	v_pk_add_f32 v[12:13], v[80:81], v[12:13]
	global_store_dwordx4 v[100:101], v[10:13], off offset:-4096
	v_lshlrev_b32_e32 v14, 16, v156
	v_and_b32_e32 v15, 0xffff0000, v156
	v_lshlrev_b32_e32 v16, 16, v157
	v_and_b32_e32 v17, 0xffff0000, v157
	v_pk_add_f32 v[14:15], v[62:63], v[14:15]
	v_pk_add_f32 v[16:17], v[60:61], v[16:17]
	global_store_dwordx4 v[100:101], v[14:17], off offset:-3072
	v_lshlrev_b32_e32 v2, 16, v158
	v_and_b32_e32 v3, 0xffff0000, v158
	v_lshlrev_b32_e32 v4, 16, v159
	v_and_b32_e32 v5, 0xffff0000, v159
	v_pk_add_f32 v[2:3], v[58:59], v[2:3]
	v_pk_add_f32 v[4:5], v[56:57], v[4:5]
	global_store_dwordx4 v[100:101], v[2:5], off offset:-2048
	v_lshlrev_b32_e32 v10, 16, v160
	v_and_b32_e32 v11, 0xffff0000, v160
	v_lshlrev_b32_e32 v12, 16, v161
	v_and_b32_e32 v13, 0xffff0000, v161
	v_pk_add_f32 v[10:11], v[54:55], v[10:11]
	v_pk_add_f32 v[12:13], v[52:53], v[12:13]
	global_store_dwordx4 v[100:101], v[10:13], off offset:-1024
	v_lshlrev_b32_e32 v14, 16, v162
	v_and_b32_e32 v15, 0xffff0000, v162
	v_lshlrev_b32_e32 v16, 16, v163
	v_and_b32_e32 v17, 0xffff0000, v163
	v_pk_add_f32 v[14:15], v[50:51], v[14:15]
	v_pk_add_f32 v[16:17], v[48:49], v[16:17]
	global_store_dwordx4 v[100:101], v[14:17], off
	v_lshlrev_b32_e32 v2, 16, v164
	v_and_b32_e32 v3, 0xffff0000, v164
	v_lshlrev_b32_e32 v4, 16, v165
	v_and_b32_e32 v5, 0xffff0000, v165
	v_pk_add_f32 v[2:3], v[46:47], v[2:3]
	v_pk_add_f32 v[4:5], v[44:45], v[4:5]
	global_store_dwordx4 v[100:101], v[2:5], off offset:1024
	v_lshlrev_b32_e32 v10, 16, v166
	v_and_b32_e32 v11, 0xffff0000, v166
	v_lshlrev_b32_e32 v12, 16, v167
	v_and_b32_e32 v13, 0xffff0000, v167
	v_pk_add_f32 v[10:11], v[42:43], v[10:11]
	v_pk_add_f32 v[12:13], v[40:41], v[12:13]
	global_store_dwordx4 v[100:101], v[10:13], off offset:2048
	v_lshlrev_b32_e32 v14, 16, v168
	v_and_b32_e32 v15, 0xffff0000, v168
	v_lshlrev_b32_e32 v16, 16, v169
	v_and_b32_e32 v17, 0xffff0000, v169
	v_pk_add_f32 v[14:15], v[38:39], v[14:15]
	v_pk_add_f32 v[16:17], v[36:37], v[16:17]
	global_store_dwordx4 v[100:101], v[14:17], off offset:3072
	v_lshlrev_b32_e32 v2, 16, v170
	v_and_b32_e32 v3, 0xffff0000, v170
	v_lshlrev_b32_e32 v4, 16, v171
	v_and_b32_e32 v5, 0xffff0000, v171
	v_pk_add_f32 v[2:3], v[32:33], v[2:3]
	v_pk_add_f32 v[4:5], v[34:35], v[4:5]
	global_store_dwordx4 v[102:103], v[2:5], off
	v_lshlrev_b32_e32 v10, 16, v172
	v_and_b32_e32 v11, 0xffff0000, v172
	v_lshlrev_b32_e32 v12, 16, v173
	v_and_b32_e32 v13, 0xffff0000, v173
	v_pk_add_f32 v[10:11], v[30:31], v[10:11]
	v_pk_add_f32 v[12:13], v[28:29], v[12:13]
	global_store_dwordx4 v[102:103], v[10:13], off offset:1024
	v_lshlrev_b32_e32 v14, 16, v174
	v_and_b32_e32 v15, 0xffff0000, v174
	v_lshlrev_b32_e32 v16, 16, v175
	v_and_b32_e32 v17, 0xffff0000, v175
	v_pk_add_f32 v[14:15], v[26:27], v[14:15]
	v_pk_add_f32 v[16:17], v[24:25], v[16:17]
	global_store_dwordx4 v[102:103], v[14:17], off offset:2048
	v_lshlrev_b32_e32 v2, 16, v176
	v_and_b32_e32 v3, 0xffff0000, v176
	v_lshlrev_b32_e32 v4, 16, v177
	v_and_b32_e32 v5, 0xffff0000, v177
	v_pk_add_f32 v[2:3], v[20:21], v[2:3]
	v_pk_add_f32 v[4:5], v[22:23], v[4:5]
	global_store_dwordx4 v[102:103], v[2:5], off offset:3072
	s_cbranch_scc0 .LBB0_901
	s_add_i32 s2, s2, s3
	s_cmpk_gt_i32 s2, 0xff
	s_barrier
	s_cbranch_scc0 .LBB0_892

; __global__ void __launch_bounds__(NTHREADS, 2) fwd(Args args) {
	.amdhsa_kernel _Z3fwd4Args
		.amdhsa_group_segment_fixed_size 0
		.amdhsa_private_segment_fixed_size 0
		.amdhsa_kernarg_size 432
		.amdhsa_user_sgpr_count 2
		.amdhsa_user_sgpr_dispatch_ptr 0
		.amdhsa_user_sgpr_queue_ptr 0
		.amdhsa_user_sgpr_kernarg_segment_ptr 1
		.amdhsa_user_sgpr_dispatch_id 0
		.amdhsa_user_sgpr_kernarg_preload_length 0
		.amdhsa_user_sgpr_kernarg_preload_offset 0
		.amdhsa_user_sgpr_private_segment_size 0
		.amdhsa_uses_dynamic_stack 0
		.amdhsa_enable_private_segment 0
		.amdhsa_system_sgpr_workgroup_id_x 1
		.amdhsa_system_sgpr_workgroup_id_y 0
		.amdhsa_system_sgpr_workgroup_id_z 0
		.amdhsa_system_sgpr_workgroup_info 0
		.amdhsa_system_vgpr_workitem_id 0
		.amdhsa_next_free_vgpr 250
		.amdhsa_next_free_sgpr 100
		.amdhsa_accum_offset 252
		.amdhsa_reserve_vcc 1
		.amdhsa_float_round_mode_32 0
		.amdhsa_float_round_mode_16_64 0
		.amdhsa_float_denorm_mode_32 3
		.amdhsa_float_denorm_mode_16_64 3
		.amdhsa_dx10_clamp 1
		.amdhsa_ieee_mode 1
		.amdhsa_fp16_overflow 0
		.amdhsa_tg_split 0
		.amdhsa_exception_fp_ieee_invalid_op 0
		.amdhsa_exception_fp_denorm_src 0
		.amdhsa_exception_fp_ieee_div_zero 0
		.amdhsa_exception_fp_ieee_overflow 0
		.amdhsa_exception_fp_ieee_underflow 0
		.amdhsa_exception_fp_ieee_inexact 0
		.amdhsa_exception_int_div_zero 0
	.end_amdhsa_kernel

; __global__ void __launch_bounds__(NTHREADS, 2) fwd(Args args) {
amdhsa.kernels:
  - .agpr_count:     0
    .args:
      - .offset:         0
        .size:           176
        .value_kind:     by_value
      - .offset:         176
        .size:           4
        .value_kind:     hidden_block_count_x
      - .offset:         180
        .size:           4
        .value_kind:     hidden_block_count_y
      - .offset:         184
        .size:           4
        .value_kind:     hidden_block_count_z
      - .offset:         188
        .size:           2
        .value_kind:     hidden_group_size_x
      - .offset:         190
        .size:           2
        .value_kind:     hidden_group_size_y
      - .offset:         192
        .size:           2
        .value_kind:     hidden_group_size_z
      - .offset:         194
        .size:           2
        .value_kind:     hidden_remainder_x
      - .offset:         196
        .size:           2
        .value_kind:     hidden_remainder_y
      - .offset:         198
        .size:           2
        .value_kind:     hidden_remainder_z
      - .offset:         216
        .size:           8
        .value_kind:     hidden_global_offset_x
      - .offset:         224
        .size:           8
        .value_kind:     hidden_global_offset_y
      - .offset:         232
        .size:           8
        .value_kind:     hidden_global_offset_z
      - .offset:         240
        .size:           2
        .value_kind:     hidden_grid_dims
      - .offset:         296
        .size:           4
        .value_kind:     hidden_dynamic_lds_size
    .group_segment_fixed_size: 0
    .kernarg_segment_align: 8
    .kernarg_segment_size: 432
    .language:       OpenCL C
    .language_version:
      - 2
      - 0
    .max_flat_workgroup_size: 512
    .name:           _Z3fwd4Args
    .private_segment_fixed_size: 0
    .sgpr_count:     106
    .sgpr_spill_count: 42
    .symbol:         _Z3fwd4Args.kd
    .uniform_work_group_size: 1
    .uses_dynamic_stack: false
    .vgpr_count:     250
    .vgpr_spill_count: 0
    .wavefront_size: 64
